# stick-breaking attention: cross-row lane reads via v_permlane32_swap/v_permlane16_swap instead of ds_bpermute (no LDS round trip)
# baseline (speedup 1.0000x reference)
.LBB0_595:
	v_med3_f32 v44, v44, s87, v123
	v_exp_f32_e32 v44, v44
	v_lshlrev_b32_e32 v132, 2, v49
	v_med3_f32 v45, v45, s87, v123
	v_lshlrev_b32_e32 v126, 3, v127
	v_add_f32_e32 v49, 1.0, v44
	v_rcp_f32_e32 v49, v49
	v_exp_f32_e32 v45, v45
	v_lshl_add_u32 v61, s14, 6, v126
	v_add_u32_e32 v50, 32, v61
	v_cmp_lt_i32_e64 s[20:21], v50, v125
	v_med3_f32 v46, v46, s87, v123
	v_exp_f32_e32 v46, v46
	v_cndmask_b32_e64 v56, 1.0, v49, s[20:21]
	v_add_f32_e32 v49, 1.0, v45
	v_rcp_f32_e32 v49, v49
	v_add_u32_e32 v50, 33, v61
	v_cmp_lt_i32_e64 s[22:23], v50, v125
	v_med3_f32 v47, v47, s87, v123
	v_exp_f32_e32 v47, v47
	v_cndmask_b32_e64 v55, 1.0, v49, s[22:23]
	v_add_f32_e32 v49, 1.0, v46
	v_rcp_f32_e32 v49, v49
	v_add_u32_e32 v50, 34, v61
	v_cmp_lt_i32_e64 s[24:25], v50, v125
	v_med3_f32 v40, v40, s87, v123
	v_exp_f32_e32 v40, v40
	v_cndmask_b32_e64 v54, 1.0, v49, s[24:25]
	v_add_f32_e32 v49, 1.0, v47
	v_rcp_f32_e32 v49, v49
	v_add_u32_e32 v50, 35, v61
	v_cmp_lt_i32_e64 s[26:27], v50, v125
	v_med3_f32 v41, v41, s87, v123
	v_exp_f32_e32 v41, v41
	v_cndmask_b32_e64 v53, 1.0, v49, s[26:27]
	v_add_f32_e32 v49, 1.0, v40
	v_rcp_f32_e32 v49, v49
	v_med3_f32 v42, v42, s87, v123
	v_add_u32_e32 v50, 36, v61
	v_exp_f32_e32 v42, v42
	v_cmp_lt_i32_e64 s[28:29], v50, v125
	v_med3_f32 v43, v43, s87, v123
	v_exp_f32_e32 v51, v43
	v_cndmask_b32_e64 v52, 1.0, v49, s[28:29]
	v_add_f32_e32 v49, 1.0, v41
	v_rcp_f32_e32 v49, v49
	v_add_f32_e32 v43, 1.0, v42
	v_add_u32_e32 v50, 37, v61
	v_rcp_f32_e32 v43, v43
	v_cmp_lt_i32_e64 s[30:31], v50, v125
	v_add_f32_e32 v57, 1.0, v51
	v_rcp_f32_e32 v57, v57
	v_cndmask_b32_e64 v50, 1.0, v49, s[30:31]
	v_add_u32_e32 v49, 38, v61
	v_cmp_lt_i32_e64 s[34:35], v49, v125
	v_or_b32_e32 v133, 64, v132
	v_or_b32_e32 v134, 0x80, v132
	v_cndmask_b32_e64 v49, 1.0, v43, s[34:35]
	v_add_u32_e32 v43, 39, v61
	v_cmp_lt_i32_e64 s[36:37], v43, v125
	v_or_b32_e32 v135, 0xc0, v132
	v_cmp_eq_u32_e64 s[14:15], 2, v127
	v_cndmask_b32_e64 v43, 1.0, v57, s[36:37]
	v_mul_f32_e32 v49, v49, v43
	v_mul_f32_e32 v50, v50, v49
	v_mul_f32_e32 v52, v52, v50
	v_mul_f32_e32 v53, v53, v52
	v_mul_f32_e32 v54, v54, v53
	v_mul_f32_e32 v55, v55, v54
	v_mul_f32_e32 v56, v56, v55
	ds_bpermute_b32 v58, v132, v56
	ds_bpermute_b32 v59, v132, v56 offset:64
	ds_bpermute_b32 v57, v132, v56 offset:128
	ds_bpermute_b32 v62, v132, v56 offset:192
	v_cmp_lt_i32_e32 vcc, 0, v127
	s_mov_b64 s[38:39], 0
	v_cmp_ne_u32_e64 s[16:17], 1, v127
	s_mov_b64 s[40:41], 0
	s_and_saveexec_b64 s[18:19], vcc
	s_xor_b64 s[18:19], exec, s[18:19]
	s_and_b64 s[40:41], s[16:17], exec
	s_or_saveexec_b64 s[42:43], s[18:19]
	v_cmp_ne_u32_e64 s[18:19], 0, v127
	s_xor_b64 exec, exec, s[42:43]
	s_andn2_b64 s[38:39], s[40:41], exec
	s_and_b64 s[40:41], s[18:19], exec
	s_or_b64 s[40:41], s[38:39], s[40:41]
	s_mov_b64 s[38:39], exec
	s_or_b64 exec, exec, s[42:43]
	s_waitcnt lgkmcnt(0)
	v_mul_f32_e32 v60, v57, v62
	v_mov_b32_e32 v57, v60
	s_and_saveexec_b64 s[42:43], s[40:41]
	s_xor_b64 s[40:41], exec, s[42:43]
	v_cndmask_b32_e64 v57, 1.0, v62, s[14:15]
	s_andn2_b64 s[38:39], s[38:39], exec
	s_or_b64 exec, exec, s[40:41]
	s_and_saveexec_b64 s[40:41], s[38:39]
	v_mul_f32_e32 v57, v60, v59
	s_or_b64 exec, exec, s[40:41]
	v_med3_f32 v36, v36, s87, v123
	v_exp_f32_e32 v36, v36
	v_med3_f32 v37, v37, s87, v123
	v_exp_f32_e32 v37, v37
	v_med3_f32 v38, v38, s87, v123
	v_add_f32_e32 v62, 1.0, v36
	v_rcp_f32_e32 v62, v62
	v_exp_f32_e32 v38, v38
	v_add_f32_e32 v63, 1.0, v37
	v_cmp_lt_i32_e64 s[38:39], v61, v125
	v_rcp_f32_e32 v63, v63
	v_med3_f32 v39, v39, s87, v123
	v_cndmask_b32_e64 v69, 1.0, v62, s[38:39]
	v_or_b32_e32 v62, 1, v61
	v_cmp_lt_i32_e64 s[40:41], v62, v125
	v_add_f32_e32 v62, 1.0, v38
	v_rcp_f32_e32 v62, v62
	v_exp_f32_e32 v39, v39
	v_cndmask_b32_e64 v68, 1.0, v63, s[40:41]
	v_or_b32_e32 v63, 2, v61
	v_cmp_lt_i32_e64 s[42:43], v63, v125
	v_med3_f32 v32, v32, s87, v123
	v_med3_f32 v33, v33, s87, v123
	v_cndmask_b32_e64 v67, 1.0, v62, s[42:43]
	v_add_f32_e32 v62, 1.0, v39
	v_rcp_f32_e32 v63, v62
	v_exp_f32_e32 v62, v32
	v_or_b32_e32 v32, 3, v61
	v_cmp_lt_i32_e64 s[44:45], v32, v125
	v_or_b32_e32 v64, 5, v61
	v_add_f32_e32 v32, 1.0, v62
	v_cndmask_b32_e64 v66, 1.0, v63, s[44:45]
	v_rcp_f32_e32 v32, v32
	v_exp_f32_e32 v63, v33
	v_or_b32_e32 v33, 4, v61
	v_cmp_lt_i32_e64 s[46:47], v33, v125
	v_med3_f32 v34, v34, s87, v123
	v_exp_f32_e32 v34, v34
	v_cndmask_b32_e64 v33, 1.0, v32, s[46:47]
	v_add_f32_e32 v32, 1.0, v63
	v_rcp_f32_e32 v32, v32
	v_cmp_lt_i32_e64 s[48:49], v64, v125
	v_cmp_lt_i32_e32 vcc, 0, v127
	s_mov_b64 s[68:69], 0
	v_cndmask_b32_e64 v65, 1.0, v32, s[48:49]
	v_med3_f32 v32, v35, s87, v123
	v_exp_f32_e32 v64, v32
	v_add_f32_e32 v32, 1.0, v34
	v_rcp_f32_e32 v32, v32
	v_or_b32_e32 v35, 6, v61
	v_add_f32_e32 v70, 1.0, v64
	v_rcp_f32_e32 v70, v70
	v_cmp_lt_i32_e64 s[50:51], v35, v125
	s_mov_b64 s[94:95], 0
	s_nop 0
	v_cndmask_b32_e64 v35, 1.0, v32, s[50:51]
	v_or_b32_e32 v32, 7, v61
	v_cmp_lt_i32_e64 s[52:53], v32, v125
	s_nop 1
	v_cndmask_b32_e64 v32, 1.0, v70, s[52:53]
	v_mul_f32_e32 v35, v35, v32
	v_mul_f32_e32 v61, v65, v35
	v_mul_f32_e32 v65, v33, v61
	v_mul_f32_e32 v66, v66, v65
	v_mul_f32_e32 v67, v67, v66
	v_mul_f32_e32 v68, v68, v67
	v_mul_f32_e32 v69, v69, v68
	v_mov_b32_e32 v87, v69
	v_mov_b32_e32 v70, v69
	s_nop 1
	v_permlane32_swap_b32 v87, v70
	v_mov_b32_e32 v86, v87
	v_mov_b32_e32 v33, v70
	s_nop 1
	v_permlane16_swap_b32 v86, v87
	v_permlane16_swap_b32 v33, v70
	s_nop 1
	s_and_saveexec_b64 s[96:97], vcc
	s_xor_b64 s[96:97], exec, s[96:97]
	s_and_b64 s[94:95], s[16:17], exec
	s_andn2_saveexec_b64 s[96:97], s[96:97]
	s_andn2_b64 s[68:69], s[94:95], exec
	s_and_b64 s[94:95], s[18:19], exec
	s_or_b64 s[94:95], s[68:69], s[94:95]
	s_mov_b64 s[68:69], exec
	s_or_b64 exec, exec, s[96:97]
	s_waitcnt lgkmcnt(0)
	v_mul_f32_e32 v88, v33, v70
	v_mov_b32_e32 v33, v88
	s_and_saveexec_b64 s[96:97], s[94:95]
	s_xor_b64 s[94:95], exec, s[96:97]
	v_cndmask_b32_e64 v33, 1.0, v70, s[14:15]
	s_andn2_b64 s[68:69], s[68:69], exec
	s_or_b64 exec, exec, s[94:95]
	s_and_saveexec_b64 s[94:95], s[68:69]
	v_mul_f32_e32 v33, v88, v87
	s_or_b64 exec, exec, s[94:95]
	s_and_b64 vcc, exec, s[12:13]
	s_cbranch_vccnz .LBB0_613
	s_waitcnt vmcnt(3)
	ds_write_b128 v98, v[16:19] offset:16384
	s_waitcnt vmcnt(2)
	ds_write_b128 v99, v[20:23] offset:16384
	s_waitcnt vmcnt(1)
	ds_write_b128 v100, v[24:27] offset:32768
	s_waitcnt vmcnt(0)
	ds_write_b128 v124, v[28:31] offset:32768

.LBB0_619:
	v_med3_f32 v64, v80, s87, v123
	v_exp_f32_e32 v66, v64
	v_med3_f32 v64, v81, s87, v123
	v_exp_f32_e32 v67, v64
	v_add_u32_e32 v80, s62, v126
	v_add_f32_e32 v64, 1.0, v66
	v_rcp_f32_e32 v64, v64
	v_add_u32_e32 v65, 32, v80
	v_add_f32_e32 v81, 1.0, v67
	v_cmp_lt_i32_e32 vcc, v65, v125
	v_med3_f32 v83, v83, s87, v123
	v_exp_f32_e32 v83, v83
	v_cndmask_b32_e32 v65, 1.0, v64, vcc
	v_rcp_f32_e32 v64, v81
	v_med3_f32 v81, v82, s87, v123
	v_exp_f32_e32 v82, v81
	v_add_u32_e32 v81, 33, v80
	v_cmp_lt_i32_e64 s[20:21], v81, v125
	v_add_u32_e32 v84, 34, v80
	v_cmp_lt_i32_e64 s[22:23], v84, v125
	v_cndmask_b32_e64 v81, 1.0, v64, s[20:21]
	v_add_f32_e32 v64, 1.0, v82
	v_rcp_f32_e32 v64, v64
	v_med3_f32 v76, v76, s87, v123
	v_exp_f32_e32 v76, v76
	v_add_u32_e32 v84, 35, v80
	v_cndmask_b32_e64 v94, 1.0, v64, s[22:23]
	v_add_f32_e32 v64, 1.0, v83
	v_rcp_f32_e32 v64, v64
	v_cmp_lt_i32_e64 s[24:25], v84, v125
	v_med3_f32 v77, v77, s87, v123
	v_exp_f32_e32 v77, v77
	v_cndmask_b32_e64 v92, 1.0, v64, s[24:25]
	v_add_f32_e32 v64, 1.0, v76
	v_rcp_f32_e32 v64, v64
	v_add_u32_e32 v84, 36, v80
	v_cmp_lt_i32_e64 s[26:27], v84, v125
	v_add_u32_e32 v84, 37, v80
	v_med3_f32 v78, v78, s87, v123
	v_cndmask_b32_e64 v91, 1.0, v64, s[26:27]
	v_add_f32_e32 v64, 1.0, v77
	v_rcp_f32_e32 v64, v64
	v_exp_f32_e32 v90, v78
	v_cmp_lt_i32_e64 s[28:29], v84, v125
	v_cmp_lt_i32_e64 s[36:37], 0, v127
	s_mov_b64 s[38:39], 0
	v_cndmask_b32_e64 v78, 1.0, v64, s[28:29]
	v_med3_f32 v64, v79, s87, v123
	v_exp_f32_e32 v93, v64
	v_add_f32_e32 v64, 1.0, v90
	v_rcp_f32_e32 v64, v64
	v_add_u32_e32 v79, 38, v80
	v_add_f32_e32 v84, 1.0, v93
	v_rcp_f32_e32 v84, v84
	v_cmp_lt_i32_e64 s[30:31], v79, v125
	s_mov_b64 s[40:41], 0
	s_nop 0
	v_cndmask_b32_e64 v79, 1.0, v64, s[30:31]
	v_add_u32_e32 v64, 39, v80
	v_cmp_lt_i32_e64 s[34:35], v64, v125
	s_nop 1
	v_cndmask_b32_e64 v64, 1.0, v84, s[34:35]
	v_mul_f32_e32 v84, v79, v64
	v_mul_f32_e32 v89, v78, v84
	v_mul_f32_e32 v91, v91, v89
	v_mul_f32_e32 v92, v92, v91
	v_mul_f32_e32 v94, v94, v92
	v_mul_f32_e32 v95, v81, v94
	v_mul_f32_e32 v96, v65, v95
	v_mov_b32_e32 v79, v96
	v_mov_b32_e32 v97, v96
	s_nop 1
	v_permlane32_swap_b32 v79, v97
	v_mov_b32_e32 v78, v79
	v_mov_b32_e32 v65, v97
	s_nop 1
	v_permlane16_swap_b32 v78, v79
	v_permlane16_swap_b32 v65, v97
	s_nop 1
	s_and_saveexec_b64 s[42:43], s[36:37]
	s_xor_b64 s[36:37], exec, s[42:43]
	s_and_b64 s[40:41], s[16:17], exec
	s_andn2_saveexec_b64 s[36:37], s[36:37]
	s_andn2_b64 s[38:39], s[40:41], exec
	s_and_b64 s[40:41], s[18:19], exec
	s_or_b64 s[40:41], s[38:39], s[40:41]
	s_mov_b64 s[38:39], exec
	s_or_b64 exec, exec, s[36:37]
	s_waitcnt lgkmcnt(0)
	v_mul_f32_e32 v81, v65, v97
	v_mov_b32_e32 v65, v81
	s_and_saveexec_b64 s[36:37], s[40:41]
	s_xor_b64 s[36:37], exec, s[36:37]
	v_cndmask_b32_e64 v65, 1.0, v97, s[14:15]
	s_andn2_b64 s[38:39], s[38:39], exec
	s_or_b64 exec, exec, s[36:37]
	s_and_saveexec_b64 s[36:37], s[38:39]
	v_mul_f32_e32 v65, v81, v79
	s_or_b64 exec, exec, s[36:37]
	v_cndmask_b32_e64 v155, 0, v77, s[28:29]
	v_mul_f32_e32 v77, v86, v87
	v_mul_f32_e32 v77, v77, v88
	v_cndmask_b32_e32 v66, 0, v66, vcc
	v_cndmask_b32_e64 v67, 0, v67, s[20:21]
	v_cndmask_b32_e64 v154, 0, v76, s[26:27]
	v_cndmask_b32_e64 v76, 0, v93, s[34:35]
	v_mul_f32_e32 v77, v85, v77
	v_cndmask_b32_e64 v97, 0, v82, s[22:23]
	v_cndmask_b32_e64 v153, 0, v83, s[24:25]
	v_pk_mul_f32 v[82:83], v[76:77], v[64:65]
	v_mul_f32_e32 v64, v66, v96
	v_mul_f32_e32 v65, v67, v95
	v_mul_f32_e32 v64, v64, v83
	v_mul_f32_e32 v65, v65, v83
	v_cvt_pk_bf16_f32 v64, v64, v65
	v_mul_f32_e32 v65, v97, v94
	v_mul_f32_e32 v66, v153, v92
	v_mul_f32_e32 v65, v65, v83
	v_mul_f32_e32 v66, v66, v83
	v_cvt_pk_bf16_f32 v65, v65, v66
	v_mul_f32_e32 v66, v154, v91
	v_mul_f32_e32 v67, v155, v89
	v_cndmask_b32_e64 v90, 0, v90, s[30:31]
	v_mul_f32_e32 v66, v66, v83
	v_mul_f32_e32 v67, v67, v83
	v_cvt_pk_bf16_f32 v66, v66, v67
	v_mul_f32_e32 v67, v90, v84
	v_mul_f32_e32 v67, v67, v83
	v_pk_mul_f32 v[82:83], v[82:83], v[82:83] op_sel_hi:[0,1]
	v_cvt_pk_bf16_f32 v67, v67, v83
	v_med3_f32 v72, v72, s87, v123
	v_exp_f32_e32 v72, v72
	v_med3_f32 v73, v73, s87, v123
	v_exp_f32_e32 v73, v73
	v_cmp_lt_i32_e64 s[20:21], v80, v125
	v_add_f32_e32 v76, 1.0, v72
	v_rcp_f32_e32 v76, v76
	v_add_f32_e32 v82, 1.0, v73
	v_rcp_f32_e32 v82, v82
	v_med3_f32 v74, v74, s87, v123
	v_cndmask_b32_e64 v84, 1.0, v76, s[20:21]
	v_or_b32_e32 v76, 1, v80
	v_exp_f32_e32 v74, v74
	v_cmp_lt_i32_e64 s[22:23], v76, v125
	v_med3_f32 v68, v68, s87, v123
	v_med3_f32 v75, v75, s87, v123
	v_cndmask_b32_e64 v89, 1.0, v82, s[22:23]
	v_or_b32_e32 v82, 2, v80
	v_cmp_lt_i32_e64 s[24:25], v82, v125
	v_exp_f32_e32 v82, v68
	v_add_f32_e32 v76, 1.0, v74
	v_rcp_f32_e32 v76, v76
	v_exp_f32_e32 v75, v75
	v_or_b32_e32 v68, 3, v80
	v_cmp_lt_i32_e64 s[26:27], v68, v125
	v_add_f32_e32 v68, 1.0, v82
	v_med3_f32 v69, v69, s87, v123
	v_rcp_f32_e32 v68, v68
	v_exp_f32_e32 v83, v69
	v_cndmask_b32_e64 v88, 1.0, v76, s[24:25]
	v_add_f32_e32 v76, 1.0, v75
	v_or_b32_e32 v69, 4, v80
	v_rcp_f32_e32 v76, v76
	v_cmp_lt_i32_e64 s[28:29], v69, v125
	v_med3_f32 v70, v70, s87, v123
	v_exp_f32_e32 v70, v70
	v_cndmask_b32_e64 v69, 1.0, v68, s[28:29]
	v_add_f32_e32 v68, 1.0, v83
	v_rcp_f32_e32 v68, v68
	v_cndmask_b32_e64 v87, 1.0, v76, s[26:27]
	v_or_b32_e32 v76, 5, v80
	v_cmp_lt_i32_e64 s[30:31], v76, v125
	v_cmp_lt_i32_e32 vcc, 0, v127
	s_mov_b64 s[38:39], 0
	v_cndmask_b32_e64 v85, 1.0, v68, s[30:31]
	v_med3_f32 v68, v71, s87, v123
	v_exp_f32_e32 v76, v68
	v_add_f32_e32 v68, 1.0, v70
	v_rcp_f32_e32 v68, v68
	v_or_b32_e32 v71, 6, v80
	v_add_f32_e32 v86, 1.0, v76
	v_rcp_f32_e32 v86, v86
	v_cmp_lt_i32_e64 s[34:35], v71, v125
	s_mov_b64 s[40:41], 0
	s_nop 0
	v_cndmask_b32_e64 v71, 1.0, v68, s[34:35]
	v_or_b32_e32 v68, 7, v80
	v_cmp_lt_i32_e64 s[36:37], v68, v125
	s_nop 1
	v_cndmask_b32_e64 v68, 1.0, v86, s[36:37]
	v_mul_f32_e32 v71, v71, v68
	v_mul_f32_e32 v85, v85, v71
	v_mul_f32_e32 v86, v69, v85
	v_mul_f32_e32 v87, v87, v86
	v_mul_f32_e32 v88, v88, v87
	v_mul_f32_e32 v89, v89, v88
	v_mul_f32_e32 v90, v84, v89
	v_mov_b32_e32 v84, v90
	v_mov_b32_e32 v69, v90
	s_nop 1
	v_permlane32_swap_b32 v84, v69
	v_mov_b32_e32 v80, v84
	v_mov_b32_e32 v91, v69
	s_nop 1
	v_permlane16_swap_b32 v80, v84
	v_permlane16_swap_b32 v91, v69
	s_nop 1
	s_and_saveexec_b64 s[42:43], vcc
	s_xor_b64 s[42:43], exec, s[42:43]
	s_and_b64 s[40:41], s[16:17], exec
	s_andn2_saveexec_b64 s[42:43], s[42:43]
	s_andn2_b64 s[38:39], s[40:41], exec
	s_and_b64 s[40:41], s[18:19], exec
	s_or_b64 s[40:41], s[38:39], s[40:41]
	s_mov_b64 s[38:39], exec
	s_or_b64 exec, exec, s[42:43]
	s_waitcnt lgkmcnt(0)
	v_mul_f32_e32 v91, v91, v69
	v_mov_b32_e32 v92, v91
	s_and_saveexec_b64 s[42:43], s[40:41]
	s_xor_b64 s[40:41], exec, s[42:43]
	v_cndmask_b32_e64 v92, 1.0, v69, s[14:15]
	s_andn2_b64 s[38:39], s[38:39], exec
	s_or_b64 exec, exec, s[40:41]
	s_and_saveexec_b64 s[40:41], s[38:39]
	v_mul_f32_e32 v92, v91, v84
	s_or_b64 exec, exec, s[40:41]
	s_and_b64 vcc, exec, s[12:13]
	s_cbranch_vccnz .LBB0_637
	s_waitcnt vmcnt(3)
	ds_write_b128 v98, v[16:19]
	s_waitcnt vmcnt(2)
	ds_write_b128 v99, v[20:23]
	s_waitcnt vmcnt(1)
	ds_write_b128 v100, v[24:27] offset:49152
	s_waitcnt vmcnt(0)
	ds_write_b128 v124, v[28:31] offset:49152

.LBB0_643:
	v_med3_f32 v66, v86, s87, v123
	v_med3_f32 v69, v81, s87, v123
	v_exp_f32_e32 v86, v66
	v_med3_f32 v66, v87, s87, v123
	v_exp_f32_e32 v89, v69
	v_med3_f32 v69, v82, s87, v123
	v_exp_f32_e32 v87, v66
	v_med3_f32 v66, v80, s87, v123
	v_exp_f32_e32 v80, v69
	v_med3_f32 v69, v83, s87, v123
	v_exp_f32_e32 v81, v69
	v_exp_f32_e32 v88, v66
	v_med3_f32 v64, v84, s87, v123
	v_exp_f32_e32 v84, v64
	v_med3_f32 v64, v85, s87, v123
	v_add_f32_e32 v70, 1.0, v80
	v_add_f32_e32 v71, 1.0, v81
	v_exp_f32_e32 v85, v64
	v_add_f32_e32 v69, 1.0, v89
	v_rcp_f32_e32 v70, v70
	v_rcp_f32_e32 v83, v71
	v_add_f32_e32 v68, 1.0, v88
	v_rcp_f32_e32 v69, v69
	v_add_f32_e32 v67, 1.0, v87
	v_rcp_f32_e32 v68, v68
	v_add_f32_e32 v66, 1.0, v86
	v_rcp_f32_e32 v67, v67
	v_add_f32_e32 v65, 1.0, v85
	v_rcp_f32_e32 v66, v66
	v_mul_f32_e32 v82, v70, v83
	v_add_f32_e32 v64, 1.0, v84
	v_rcp_f32_e32 v65, v65
	v_mul_f32_e32 v91, v69, v82
	v_rcp_f32_e32 v64, v64
	v_mul_f32_e32 v90, v68, v91
	v_mul_f32_e32 v93, v67, v90
	v_mul_f32_e32 v92, v66, v93
	v_mul_f32_e32 v95, v65, v92
	v_mul_f32_e32 v94, v64, v95
	v_mov_b32_e32 v71, v94
	v_mov_b32_e32 v64, v94
	s_nop 1
	v_permlane32_swap_b32 v71, v64
	v_mov_b32_e32 v70, v71
	v_mov_b32_e32 v65, v64
	s_nop 1
	v_permlane16_swap_b32 v70, v71
	v_permlane16_swap_b32 v65, v64
	s_nop 1
	s_waitcnt lgkmcnt(0)
	v_mul_f32_e32 v157, v65, v64
	v_mul_f32_e32 v246, v157, v71
	v_cndmask_b32_e64 v158, 1.0, v64, s[14:15]
	v_cndmask_b32_e64 v158, v246, v158, s[18:19]
	v_cndmask_b32_e64 v158, v157, v158, s[16:17]
	v_med3_f32 v64, v76, s87, v123
	v_exp_f32_e32 v66, v64
	v_med3_f32 v64, v77, s87, v123
	v_exp_f32_e32 v67, v64
	v_med3_f32 v72, v72, s87, v123
	v_add_f32_e32 v64, 1.0, v66
	v_rcp_f32_e32 v68, v64
	v_med3_f32 v64, v78, s87, v123
	v_exp_f32_e32 v64, v64
	v_exp_f32_e32 v76, v72
	v_add_f32_e32 v65, 1.0, v67
	v_rcp_f32_e32 v69, v65
	v_add_f32_e32 v72, 1.0, v64
	v_rcp_f32_e32 v96, v72
	v_med3_f32 v72, v73, s87, v123
	v_exp_f32_e32 v77, v72
	v_med3_f32 v72, v74, s87, v123
	v_exp_f32_e32 v72, v72
	v_med3_f32 v73, v75, s87, v123
	v_exp_f32_e32 v73, v73
	v_med3_f32 v65, v79, s87, v123
	v_exp_f32_e32 v65, v65
	v_add_f32_e32 v75, 1.0, v72
	v_rcp_f32_e32 v97, v75
	v_add_f32_e32 v75, 1.0, v73
	v_add_f32_e32 v74, 1.0, v77
	v_rcp_f32_e32 v75, v75
	v_add_f32_e32 v79, 1.0, v76
	v_rcp_f32_e32 v154, v74
	v_add_f32_e32 v78, 1.0, v65
	v_rcp_f32_e32 v155, v79
	v_rcp_f32_e32 v156, v78
	v_mul_f32_e32 v74, v97, v75
	v_mul_f32_e32 v79, v154, v74
	v_mul_f32_e32 v78, v155, v79
	v_mul_f32_e32 v97, v156, v78
	v_mul_f32_e32 v96, v96, v97
	v_mul_f32_e32 v69, v69, v96
	v_mul_f32_e32 v68, v68, v69
	v_mov_b32_e32 v155, v68
	v_mov_b32_e32 v160, v68
	s_nop 1
	v_permlane32_swap_b32 v155, v160
	v_mov_b32_e32 v154, v155
	v_mov_b32_e32 v156, v160
	s_nop 1
	v_permlane16_swap_b32 v154, v155
	v_permlane16_swap_b32 v156, v160
	s_nop 1
	s_waitcnt lgkmcnt(0)
	v_mul_f32_e32 v156, v156, v160
	v_mul_f32_e32 v246, v156, v155
	v_cndmask_b32_e64 v159, 1.0, v160, s[14:15]
	v_cndmask_b32_e64 v159, v246, v159, s[18:19]
	v_cndmask_b32_e64 v159, v156, v159, s[16:17]
	s_and_b64 vcc, exec, s[12:13]
	s_cbranch_vccnz .LBB0_661
	s_waitcnt vmcnt(3)
	ds_write_b128 v98, v[16:19] offset:16384
	s_waitcnt vmcnt(2)
	ds_write_b128 v99, v[20:23] offset:16384
	s_waitcnt vmcnt(1)
	ds_write_b128 v100, v[24:27] offset:32768
	s_waitcnt vmcnt(0)
	ds_write_b128 v124, v[28:31] offset:32768

.LBB0_667:
	v_med3_f32 v73, v73, s87, v123
	v_exp_f32_e32 v73, v73
	v_med3_f32 v78, v78, s87, v123
	v_exp_f32_e32 v78, v78
	v_med3_f32 v79, v79, s87, v123
	v_med3_f32 v72, v72, s87, v123
	v_med3_f32 v77, v77, s87, v123
	v_exp_f32_e32 v79, v79
	v_exp_f32_e32 v72, v72
	v_med3_f32 v74, v74, s87, v123
	v_med3_f32 v76, v76, s87, v123
	v_exp_f32_e32 v77, v77
	v_add_f32_e32 v81, 1.0, v73
	v_exp_f32_e32 v74, v74
	v_med3_f32 v75, v75, s87, v123
	v_exp_f32_e32 v76, v76
	v_rcp_f32_e32 v87, v81
	v_exp_f32_e32 v75, v75
	v_add_f32_e32 v81, 1.0, v78
	v_rcp_f32_e32 v85, v81
	v_add_f32_e32 v81, 1.0, v79
	v_add_f32_e32 v80, 1.0, v72
	v_add_f32_e32 v83, 1.0, v77
	v_rcp_f32_e32 v81, v81
	v_rcp_f32_e32 v86, v80
	v_add_f32_e32 v80, 1.0, v74
	v_add_f32_e32 v82, 1.0, v76
	v_rcp_f32_e32 v83, v83
	v_rcp_f32_e32 v84, v80
	v_add_f32_e32 v80, 1.0, v75
	v_rcp_f32_e32 v82, v82
	v_rcp_f32_e32 v88, v80
	v_mul_f32_e32 v80, v85, v81
	v_mul_f32_e32 v83, v83, v80
	v_mul_f32_e32 v82, v82, v83
	v_mul_f32_e32 v85, v88, v82
	v_mul_f32_e32 v84, v84, v85
	v_mul_f32_e32 v87, v87, v84
	v_mul_f32_e32 v86, v86, v87
	v_mov_b32_e32 v97, v86
	v_mov_b32_e32 v88, v86
	s_nop 1
	v_permlane32_swap_b32 v97, v88
	v_mov_b32_e32 v96, v97
	v_mov_b32_e32 v89, v88
	s_nop 1
	v_permlane16_swap_b32 v96, v97
	v_permlane16_swap_b32 v89, v88
	s_nop 1
	s_waitcnt lgkmcnt(0)
	v_mul_f32_e32 v159, v89, v88
	v_mul_f32_e32 v246, v159, v97
	v_cndmask_b32_e64 v158, 1.0, v88, s[14:15]
	v_cndmask_b32_e64 v158, v246, v158, s[18:19]
	v_cndmask_b32_e64 v158, v159, v158, s[16:17]
	v_med3_f32 v69, v69, s87, v123
	v_exp_f32_e32 v69, v69
	v_med3_f32 v66, v66, s87, v123
	v_exp_f32_e32 v66, v66
	v_med3_f32 v67, v67, s87, v123
	v_med3_f32 v68, v68, s87, v123
	v_med3_f32 v65, v65, s87, v123
	v_exp_f32_e32 v67, v67
	v_exp_f32_e32 v68, v68
	v_med3_f32 v70, v70, s87, v123
	v_med3_f32 v64, v64, s87, v123
	v_exp_f32_e32 v65, v65
	v_add_f32_e32 v89, 1.0, v69
	v_exp_f32_e32 v70, v70
	v_med3_f32 v71, v71, s87, v123
	v_exp_f32_e32 v64, v64
	v_rcp_f32_e32 v95, v89
	v_exp_f32_e32 v71, v71
	v_add_f32_e32 v89, 1.0, v66
	v_rcp_f32_e32 v93, v89
	v_add_f32_e32 v89, 1.0, v67
	v_add_f32_e32 v88, 1.0, v68
	v_add_f32_e32 v91, 1.0, v65
	v_rcp_f32_e32 v89, v89
	v_rcp_f32_e32 v94, v88
	v_add_f32_e32 v88, 1.0, v70
	v_add_f32_e32 v90, 1.0, v64
	v_rcp_f32_e32 v91, v91
	v_rcp_f32_e32 v92, v88
	v_add_f32_e32 v88, 1.0, v71
	v_rcp_f32_e32 v90, v90
	v_rcp_f32_e32 v160, v88
	v_mul_f32_e32 v88, v93, v89
	v_mul_f32_e32 v91, v91, v88
	v_mul_f32_e32 v90, v90, v91
	v_mul_f32_e32 v93, v160, v90
	v_mul_f32_e32 v92, v92, v93
	v_mul_f32_e32 v95, v95, v92
	v_mul_f32_e32 v94, v94, v95
	v_mov_b32_e32 v161, v94
	v_mov_b32_e32 v162, v94
	s_nop 1
	v_permlane32_swap_b32 v161, v162
	v_mov_b32_e32 v160, v161
	v_mov_b32_e32 v163, v162
	s_nop 1
	v_permlane16_swap_b32 v160, v161
	v_permlane16_swap_b32 v163, v162
	s_nop 1
	s_waitcnt lgkmcnt(0)
	v_mul_f32_e32 v163, v163, v162
	v_mul_f32_e32 v246, v163, v161
	v_cndmask_b32_e64 v164, 1.0, v162, s[14:15]
	v_cndmask_b32_e64 v164, v246, v164, s[18:19]
	v_cndmask_b32_e64 v164, v163, v164, s[16:17]
	s_and_b64 vcc, exec, s[12:13]
	s_cbranch_vccnz .LBB0_685
	s_waitcnt vmcnt(3)
	ds_write_b128 v98, v[16:19]
	s_waitcnt vmcnt(2)
	ds_write_b128 v99, v[20:23]
	s_waitcnt vmcnt(1)
	ds_write_b128 v100, v[24:27] offset:49152
	s_waitcnt vmcnt(0)
	ds_write_b128 v124, v[28:31] offset:49152

.LBB0_721:
	v_med3_f32 v72, v80, s87, v123
	v_exp_f32_e32 v80, v72
	v_med3_f32 v72, v81, s87, v123
	v_exp_f32_e32 v81, v72
	v_add_u32_e32 v75, s1, v126
	v_add_f32_e32 v72, 1.0, v80
	v_rcp_f32_e32 v72, v72
	v_add_u32_e32 v73, 32, v75
	v_add_f32_e32 v74, 1.0, v81
	v_cmp_lt_i32_e64 s[20:21], v73, v125
	v_med3_f32 v83, v83, s87, v123
	v_exp_f32_e32 v83, v83
	v_cndmask_b32_e64 v73, 1.0, v72, s[20:21]
	v_rcp_f32_e32 v72, v74
	v_med3_f32 v74, v82, s87, v123
	v_exp_f32_e32 v82, v74
	v_add_u32_e32 v74, 33, v75
	v_cmp_lt_i32_e64 s[22:23], v74, v125
	v_add_u32_e32 v84, 34, v75
	v_cmp_lt_i32_e64 s[24:25], v84, v125
	v_cndmask_b32_e64 v74, 1.0, v72, s[22:23]
	v_add_f32_e32 v72, 1.0, v82
	v_rcp_f32_e32 v72, v72
	v_med3_f32 v76, v76, s87, v123
	v_exp_f32_e32 v76, v76
	v_add_u32_e32 v84, 35, v75
	v_cndmask_b32_e64 v92, 1.0, v72, s[24:25]
	v_add_f32_e32 v72, 1.0, v83
	v_rcp_f32_e32 v72, v72
	v_cmp_lt_i32_e64 s[26:27], v84, v125
	v_med3_f32 v77, v77, s87, v123
	v_exp_f32_e32 v77, v77
	v_cndmask_b32_e64 v91, 1.0, v72, s[26:27]
	v_add_f32_e32 v72, 1.0, v76
	v_rcp_f32_e32 v72, v72
	v_add_u32_e32 v84, 36, v75
	v_cmp_lt_i32_e64 s[28:29], v84, v125
	v_add_u32_e32 v90, 37, v75
	v_med3_f32 v78, v78, s87, v123
	v_cndmask_b32_e64 v89, 1.0, v72, s[28:29]
	v_add_f32_e32 v72, 1.0, v77
	v_rcp_f32_e32 v72, v72
	v_exp_f32_e32 v84, v78
	v_cmp_lt_i32_e64 s[30:31], v90, v125
	v_add_u32_e32 v78, 38, v75
	v_cmp_lt_i32_e64 s[34:35], v78, v125
	v_cndmask_b32_e64 v93, 1.0, v72, s[30:31]
	v_med3_f32 v72, v79, s87, v123
	v_exp_f32_e32 v90, v72
	v_add_f32_e32 v72, 1.0, v84
	v_rcp_f32_e32 v72, v72
	v_cmp_lt_i32_e32 vcc, 0, v127
	v_add_f32_e32 v79, 1.0, v90
	v_rcp_f32_e32 v79, v79
	v_cndmask_b32_e64 v78, 1.0, v72, s[34:35]
	v_add_u32_e32 v72, 39, v75
	v_cmp_lt_i32_e64 s[36:37], v72, v125
	s_mov_b64 s[38:39], 0
	s_mov_b64 s[40:41], 0
	v_cndmask_b32_e64 v72, 1.0, v79, s[36:37]
	v_mul_f32_e32 v78, v78, v72
	v_mul_f32_e32 v79, v93, v78
	v_mul_f32_e32 v89, v89, v79
	v_mul_f32_e32 v91, v91, v89
	v_mul_f32_e32 v92, v92, v91
	v_mul_f32_e32 v93, v74, v92
	v_mul_f32_e32 v94, v73, v93
	v_mov_b32_e32 v95, v94
	v_mov_b32_e32 v97, v94
	s_nop 1
	v_permlane32_swap_b32 v95, v97
	v_mov_b32_e32 v74, v95
	v_mov_b32_e32 v73, v97
	s_nop 1
	v_permlane16_swap_b32 v74, v95
	v_permlane16_swap_b32 v73, v97
	s_nop 1
	s_and_saveexec_b64 s[42:43], vcc
	s_xor_b64 s[42:43], exec, s[42:43]
	s_and_b64 s[40:41], s[16:17], exec
	s_andn2_saveexec_b64 s[42:43], s[42:43]
	s_andn2_b64 s[38:39], s[40:41], exec
	s_and_b64 s[40:41], s[18:19], exec
	s_or_b64 s[40:41], s[38:39], s[40:41]
	s_mov_b64 s[38:39], exec
	s_or_b64 exec, exec, s[42:43]
	s_waitcnt lgkmcnt(0)
	v_mul_f32_e32 v96, v73, v97
	v_mov_b32_e32 v73, v96
	s_and_saveexec_b64 s[42:43], s[40:41]
	s_xor_b64 s[40:41], exec, s[42:43]
	v_cndmask_b32_e64 v73, 1.0, v97, s[14:15]
	s_andn2_b64 s[38:39], s[38:39], exec
	s_or_b64 exec, exec, s[40:41]
	s_and_saveexec_b64 s[40:41], s[38:39]
	v_mul_f32_e32 v73, v96, v95
	s_or_b64 exec, exec, s[40:41]
	v_med3_f32 v71, v71, s87, v123
	v_exp_f32_e32 v71, v71
	v_or_b32_e32 v155, 2, v75
	v_cmp_lt_i32_e64 s[42:43], v155, v125
	v_med3_f32 v64, v64, s87, v123
	v_add_f32_e32 v155, 1.0, v71
	v_rcp_f32_e32 v156, v155
	v_exp_f32_e32 v155, v64
	v_or_b32_e32 v64, 3, v75
	v_cmp_lt_i32_e64 s[44:45], v64, v125
	v_med3_f32 v65, v65, s87, v123
	v_add_f32_e32 v64, 1.0, v155
	v_cndmask_b32_e64 v160, 1.0, v156, s[44:45]
	v_rcp_f32_e32 v64, v64
	v_exp_f32_e32 v156, v65
	v_or_b32_e32 v65, 4, v75
	v_cmp_lt_i32_e64 s[46:47], v65, v125
	v_or_b32_e32 v157, 5, v75
	v_med3_f32 v66, v66, s87, v123
	v_cndmask_b32_e64 v65, 1.0, v64, s[46:47]
	v_add_f32_e32 v64, 1.0, v156
	v_rcp_f32_e32 v64, v64
	v_exp_f32_e32 v66, v66
	v_cmp_lt_i32_e64 s[48:49], v157, v125
	v_med3_f32 v70, v70, s87, v123
	v_med3_f32 v69, v69, s87, v123
	v_cndmask_b32_e64 v157, 1.0, v64, s[48:49]
	v_med3_f32 v64, v67, s87, v123
	v_exp_f32_e32 v158, v64
	v_add_f32_e32 v64, 1.0, v66
	v_rcp_f32_e32 v64, v64
	v_exp_f32_e32 v70, v70
	v_add_f32_e32 v159, 1.0, v158
	v_med3_f32 v68, v68, s87, v123
	v_exp_f32_e32 v69, v69
	v_or_b32_e32 v67, 6, v75
	v_rcp_f32_e32 v159, v159
	v_exp_f32_e32 v68, v68
	v_cmp_lt_i32_e64 s[50:51], v67, v125
	v_or_b32_e32 v154, 1, v75
	v_cmp_lt_i32_e64 s[40:41], v154, v125
	v_cndmask_b32_e64 v67, 1.0, v64, s[50:51]
	v_or_b32_e32 v64, 7, v75
	v_add_f32_e32 v154, 1.0, v70
	v_cmp_lt_i32_e64 s[52:53], v64, v125
	v_add_f32_e32 v153, 1.0, v69
	v_rcp_f32_e32 v154, v154
	v_cndmask_b32_e64 v64, 1.0, v159, s[52:53]
	v_add_f32_e32 v97, 1.0, v68
	v_rcp_f32_e32 v153, v153
	v_mul_f32_e32 v67, v67, v64
	v_rcp_f32_e32 v97, v97
	v_mul_f32_e32 v157, v157, v67
	v_mul_f32_e32 v159, v65, v157
	v_cndmask_b32_e64 v154, 1.0, v154, s[42:43]
	v_mul_f32_e32 v160, v160, v159
	v_cmp_lt_i32_e64 s[38:39], v75, v125
	v_cndmask_b32_e64 v153, 1.0, v153, s[40:41]
	v_mul_f32_e32 v161, v154, v160
	v_cndmask_b32_e64 v97, 1.0, v97, s[38:39]
	v_mul_f32_e32 v162, v153, v161
	v_mul_f32_e32 v163, v97, v162
	v_mov_b32_e32 v153, v163
	v_mov_b32_e32 v65, v163
	s_nop 1
	v_permlane32_swap_b32 v153, v65
	v_mov_b32_e32 v97, v153
	v_mov_b32_e32 v75, v65
	s_nop 1
	v_permlane16_swap_b32 v97, v153
	v_permlane16_swap_b32 v75, v65
	s_nop 1
	v_cmp_lt_i32_e32 vcc, 0, v127
	s_mov_b64 s[68:69], 0
	s_mov_b64 s[94:95], 0
	s_and_saveexec_b64 s[96:97], vcc
	s_xor_b64 s[96:97], exec, s[96:97]
	s_and_b64 s[94:95], s[16:17], exec
	s_andn2_saveexec_b64 s[96:97], s[96:97]
	s_andn2_b64 s[68:69], s[94:95], exec
	s_and_b64 s[94:95], s[18:19], exec
	s_or_b64 s[94:95], s[68:69], s[94:95]
	s_mov_b64 s[68:69], exec
	s_or_b64 exec, exec, s[96:97]
	s_waitcnt lgkmcnt(0)
	v_mul_f32_e32 v154, v75, v65
	v_mov_b32_e32 v164, v154
	s_and_saveexec_b64 s[96:97], s[94:95]
	s_xor_b64 s[94:95], exec, s[96:97]
	v_cndmask_b32_e64 v164, 1.0, v65, s[14:15]
	s_andn2_b64 s[68:69], s[68:69], exec
	s_or_b64 exec, exec, s[94:95]
	s_and_saveexec_b64 s[94:95], s[68:69]
	v_mul_f32_e32 v164, v154, v153
	s_or_b64 exec, exec, s[94:95]
	s_and_b64 vcc, exec, s[12:13]
	s_cbranch_vccnz .LBB0_739
	s_waitcnt vmcnt(3)
	ds_write_b128 v98, v[16:19]
	s_waitcnt vmcnt(2)
	ds_write_b128 v99, v[20:23]
	s_waitcnt vmcnt(1)
	ds_write_b128 v100, v[24:27] offset:49152
	s_waitcnt vmcnt(0)
	ds_write_b128 v124, v[28:31] offset:49152

.LBB0_770:
	v_med3_f32 v73, v73, s87, v123
	v_exp_f32_e32 v73, v73
	v_med3_f32 v78, v78, s87, v123
	v_exp_f32_e32 v78, v78
	v_med3_f32 v79, v79, s87, v123
	v_med3_f32 v72, v72, s87, v123
	v_med3_f32 v77, v77, s87, v123
	v_exp_f32_e32 v79, v79
	v_exp_f32_e32 v72, v72
	v_med3_f32 v74, v74, s87, v123
	v_med3_f32 v76, v76, s87, v123
	v_exp_f32_e32 v77, v77
	v_add_f32_e32 v81, 1.0, v73
	v_exp_f32_e32 v74, v74
	v_med3_f32 v75, v75, s87, v123
	v_exp_f32_e32 v76, v76
	v_rcp_f32_e32 v87, v81
	v_exp_f32_e32 v75, v75
	v_add_f32_e32 v81, 1.0, v78
	v_rcp_f32_e32 v85, v81
	v_add_f32_e32 v81, 1.0, v79
	v_add_f32_e32 v80, 1.0, v72
	v_add_f32_e32 v83, 1.0, v77
	v_rcp_f32_e32 v81, v81
	v_rcp_f32_e32 v86, v80
	v_add_f32_e32 v80, 1.0, v74
	v_add_f32_e32 v82, 1.0, v76
	v_rcp_f32_e32 v83, v83
	v_rcp_f32_e32 v84, v80
	v_add_f32_e32 v80, 1.0, v75
	v_rcp_f32_e32 v82, v82
	v_rcp_f32_e32 v88, v80
	v_mul_f32_e32 v80, v85, v81
	v_mul_f32_e32 v83, v83, v80
	v_mul_f32_e32 v82, v82, v83
	v_mul_f32_e32 v85, v88, v82
	v_mul_f32_e32 v84, v84, v85
	v_mul_f32_e32 v87, v87, v84
	v_mul_f32_e32 v86, v86, v87
	v_mov_b32_e32 v97, v86
	v_mov_b32_e32 v88, v86
	s_nop 1
	v_permlane32_swap_b32 v97, v88
	v_mov_b32_e32 v96, v97
	v_mov_b32_e32 v89, v88
	s_nop 1
	v_permlane16_swap_b32 v96, v97
	v_permlane16_swap_b32 v89, v88
	s_nop 1
	s_waitcnt lgkmcnt(0)
	v_mul_f32_e32 v159, v89, v88
	v_mul_f32_e32 v246, v159, v97
	v_cndmask_b32_e64 v158, 1.0, v88, s[14:15]
	v_cndmask_b32_e64 v158, v246, v158, s[18:19]
	v_cndmask_b32_e64 v158, v159, v158, s[16:17]
	v_med3_f32 v69, v69, s87, v123
	v_exp_f32_e32 v69, v69
	v_med3_f32 v68, v68, s87, v123
	v_exp_f32_e32 v68, v68
	v_med3_f32 v65, v65, s87, v123
	v_add_f32_e32 v89, 1.0, v69
	v_rcp_f32_e32 v161, v89
	v_exp_f32_e32 v89, v65
	v_med3_f32 v65, v66, s87, v123
	v_exp_f32_e32 v90, v65
	v_med3_f32 v65, v67, s87, v123
	v_exp_f32_e32 v91, v65
	v_add_f32_e32 v88, 1.0, v68
	v_med3_f32 v64, v64, s87, v123
	v_rcp_f32_e32 v160, v88
	v_med3_f32 v71, v71, s87, v123
	v_exp_f32_e32 v88, v64
	v_med3_f32 v70, v70, s87, v123
	v_exp_f32_e32 v71, v71
	v_exp_f32_e32 v70, v70
	v_add_f32_e32 v66, 1.0, v90
	v_add_f32_e32 v67, 1.0, v91
	v_add_f32_e32 v65, 1.0, v89
	v_rcp_f32_e32 v66, v66
	v_rcp_f32_e32 v93, v67
	v_add_f32_e32 v94, 1.0, v88
	v_rcp_f32_e32 v65, v65
	v_add_f32_e32 v92, 1.0, v71
	v_rcp_f32_e32 v94, v94
	v_add_f32_e32 v64, 1.0, v70
	v_rcp_f32_e32 v95, v92
	v_rcp_f32_e32 v64, v64
	v_mul_f32_e32 v92, v66, v93
	v_mul_f32_e32 v67, v65, v92
	v_mul_f32_e32 v66, v94, v67
	v_mul_f32_e32 v95, v95, v66
	v_mul_f32_e32 v94, v64, v95
	v_mul_f32_e32 v65, v161, v94
	v_mul_f32_e32 v64, v160, v65
	v_mov_b32_e32 v161, v64
	v_mov_b32_e32 v162, v64
	s_nop 1
	v_permlane32_swap_b32 v161, v162
	v_mov_b32_e32 v160, v161
	v_mov_b32_e32 v163, v162
	s_nop 1
	v_permlane16_swap_b32 v160, v161
	v_permlane16_swap_b32 v163, v162
	s_nop 1
	s_waitcnt lgkmcnt(0)
	v_mul_f32_e32 v163, v163, v162
	v_mul_f32_e32 v246, v163, v161
	v_cndmask_b32_e64 v164, 1.0, v162, s[14:15]
	v_cndmask_b32_e64 v164, v246, v164, s[18:19]
	v_cndmask_b32_e64 v164, v163, v164, s[16:17]
	s_and_b64 vcc, exec, s[12:13]
	s_cbranch_vccnz .LBB0_788
	s_waitcnt vmcnt(3)
	ds_write_b128 v98, v[16:19]
	s_waitcnt vmcnt(2)
	ds_write_b128 v99, v[20:23]
	s_waitcnt vmcnt(1)
	ds_write_b128 v100, v[24:27] offset:49152
	s_waitcnt vmcnt(0)
	ds_write_b128 v124, v[28:31] offset:49152

.LBB0_1986:
	v_med3_f32 v44, v44, s55, v123
	v_exp_f32_e32 v44, v44
	v_lshlrev_b32_e32 v132, 2, v49
	v_med3_f32 v45, v45, s55, v123
	v_lshlrev_b32_e32 v126, 3, v127
	v_add_f32_e32 v49, 1.0, v44
	v_rcp_f32_e32 v49, v49
	v_exp_f32_e32 v45, v45
	v_lshl_add_u32 v61, s10, 6, v126
	v_add_u32_e32 v50, 32, v61
	v_cmp_lt_i32_e64 s[16:17], v50, v125
	v_med3_f32 v46, v46, s55, v123
	v_exp_f32_e32 v46, v46
	v_cndmask_b32_e64 v56, 1.0, v49, s[16:17]
	v_add_f32_e32 v49, 1.0, v45
	v_rcp_f32_e32 v49, v49
	v_add_u32_e32 v50, 33, v61
	v_cmp_lt_i32_e64 s[18:19], v50, v125
	v_med3_f32 v47, v47, s55, v123
	v_exp_f32_e32 v47, v47
	v_cndmask_b32_e64 v55, 1.0, v49, s[18:19]
	v_add_f32_e32 v49, 1.0, v46
	v_rcp_f32_e32 v49, v49
	v_add_u32_e32 v50, 34, v61
	v_cmp_lt_i32_e64 s[20:21], v50, v125
	v_med3_f32 v40, v40, s55, v123
	v_exp_f32_e32 v40, v40
	v_cndmask_b32_e64 v54, 1.0, v49, s[20:21]
	v_add_f32_e32 v49, 1.0, v47
	v_rcp_f32_e32 v49, v49
	v_add_u32_e32 v50, 35, v61
	v_cmp_lt_i32_e64 s[22:23], v50, v125
	v_med3_f32 v41, v41, s55, v123
	v_exp_f32_e32 v41, v41
	v_cndmask_b32_e64 v53, 1.0, v49, s[22:23]
	v_add_f32_e32 v49, 1.0, v40
	v_rcp_f32_e32 v49, v49
	v_med3_f32 v42, v42, s55, v123
	v_add_u32_e32 v50, 36, v61
	v_exp_f32_e32 v42, v42
	v_cmp_lt_i32_e64 s[24:25], v50, v125
	v_med3_f32 v43, v43, s55, v123
	v_exp_f32_e32 v51, v43
	v_cndmask_b32_e64 v52, 1.0, v49, s[24:25]
	v_add_f32_e32 v49, 1.0, v41
	v_rcp_f32_e32 v49, v49
	v_add_f32_e32 v43, 1.0, v42
	v_add_u32_e32 v50, 37, v61
	v_rcp_f32_e32 v43, v43
	v_cmp_lt_i32_e64 s[26:27], v50, v125
	v_add_f32_e32 v57, 1.0, v51
	v_rcp_f32_e32 v57, v57
	v_cndmask_b32_e64 v50, 1.0, v49, s[26:27]
	v_add_u32_e32 v49, 38, v61
	v_cmp_lt_i32_e64 s[28:29], v49, v125
	v_or_b32_e32 v133, 64, v132
	v_or_b32_e32 v134, 0x80, v132
	v_cndmask_b32_e64 v49, 1.0, v43, s[28:29]
	v_add_u32_e32 v43, 39, v61
	v_cmp_lt_i32_e64 s[30:31], v43, v125
	v_or_b32_e32 v135, 0xc0, v132
	v_cmp_eq_u32_e64 s[10:11], 2, v127
	v_cndmask_b32_e64 v43, 1.0, v57, s[30:31]
	v_mul_f32_e32 v49, v49, v43
	v_mul_f32_e32 v50, v50, v49
	v_mul_f32_e32 v52, v52, v50
	v_mul_f32_e32 v53, v53, v52
	v_mul_f32_e32 v54, v54, v53
	v_mul_f32_e32 v55, v55, v54
	v_mul_f32_e32 v56, v56, v55
	ds_bpermute_b32 v58, v132, v56
	ds_bpermute_b32 v59, v132, v56 offset:64
	ds_bpermute_b32 v57, v132, v56 offset:128
	ds_bpermute_b32 v62, v132, v56 offset:192
	v_cmp_lt_i32_e32 vcc, 0, v127
	s_mov_b64 s[34:35], 0
	v_cmp_ne_u32_e64 s[12:13], 1, v127
	s_mov_b64 s[36:37], 0
	s_and_saveexec_b64 s[14:15], vcc
	s_xor_b64 s[14:15], exec, s[14:15]
	s_and_b64 s[36:37], s[12:13], exec
	s_or_saveexec_b64 s[38:39], s[14:15]
	v_cmp_ne_u32_e64 s[14:15], 0, v127
	s_xor_b64 exec, exec, s[38:39]
	s_andn2_b64 s[34:35], s[36:37], exec
	s_and_b64 s[36:37], s[14:15], exec
	s_or_b64 s[36:37], s[34:35], s[36:37]
	s_mov_b64 s[34:35], exec
	s_or_b64 exec, exec, s[38:39]
	s_waitcnt lgkmcnt(0)
	v_mul_f32_e32 v60, v57, v62
	v_mov_b32_e32 v57, v60
	s_and_saveexec_b64 s[38:39], s[36:37]
	s_xor_b64 s[36:37], exec, s[38:39]
	v_cndmask_b32_e64 v57, 1.0, v62, s[10:11]
	s_andn2_b64 s[34:35], s[34:35], exec
	s_or_b64 exec, exec, s[36:37]
	s_and_saveexec_b64 s[36:37], s[34:35]
	v_mul_f32_e32 v57, v60, v59
	s_or_b64 exec, exec, s[36:37]
	v_med3_f32 v36, v36, s55, v123
	v_exp_f32_e32 v36, v36
	v_med3_f32 v37, v37, s55, v123
	v_exp_f32_e32 v37, v37
	v_med3_f32 v38, v38, s55, v123
	v_add_f32_e32 v62, 1.0, v36
	v_rcp_f32_e32 v62, v62
	v_exp_f32_e32 v38, v38
	v_add_f32_e32 v63, 1.0, v37
	v_cmp_lt_i32_e64 s[34:35], v61, v125
	v_rcp_f32_e32 v63, v63
	v_med3_f32 v39, v39, s55, v123
	v_cndmask_b32_e64 v69, 1.0, v62, s[34:35]
	v_or_b32_e32 v62, 1, v61
	v_cmp_lt_i32_e64 s[36:37], v62, v125
	v_add_f32_e32 v62, 1.0, v38
	v_rcp_f32_e32 v62, v62
	v_exp_f32_e32 v39, v39
	v_cndmask_b32_e64 v68, 1.0, v63, s[36:37]
	v_or_b32_e32 v63, 2, v61
	v_cmp_lt_i32_e64 s[38:39], v63, v125
	v_med3_f32 v32, v32, s55, v123
	v_med3_f32 v33, v33, s55, v123
	v_cndmask_b32_e64 v67, 1.0, v62, s[38:39]
	v_add_f32_e32 v62, 1.0, v39
	v_rcp_f32_e32 v63, v62
	v_exp_f32_e32 v62, v32
	v_or_b32_e32 v32, 3, v61
	v_cmp_lt_i32_e64 s[40:41], v32, v125
	v_or_b32_e32 v64, 5, v61
	v_add_f32_e32 v32, 1.0, v62
	v_cndmask_b32_e64 v66, 1.0, v63, s[40:41]
	v_rcp_f32_e32 v32, v32
	v_exp_f32_e32 v63, v33
	v_or_b32_e32 v33, 4, v61
	v_cmp_lt_i32_e64 s[42:43], v33, v125
	v_med3_f32 v34, v34, s55, v123
	v_exp_f32_e32 v34, v34
	v_cndmask_b32_e64 v33, 1.0, v32, s[42:43]
	v_add_f32_e32 v32, 1.0, v63
	v_rcp_f32_e32 v32, v32
	v_cmp_lt_i32_e64 s[44:45], v64, v125
	v_cmp_lt_i32_e32 vcc, 0, v127
	s_mov_b64 s[68:69], 0
	v_cndmask_b32_e64 v65, 1.0, v32, s[44:45]
	v_med3_f32 v32, v35, s55, v123
	v_exp_f32_e32 v64, v32
	v_add_f32_e32 v32, 1.0, v34
	v_rcp_f32_e32 v32, v32
	v_or_b32_e32 v35, 6, v61
	v_add_f32_e32 v70, 1.0, v64
	v_rcp_f32_e32 v70, v70
	v_cmp_lt_i32_e64 s[46:47], v35, v125
	s_mov_b64 s[86:87], 0
	s_nop 0
	v_cndmask_b32_e64 v35, 1.0, v32, s[46:47]
	v_or_b32_e32 v32, 7, v61
	v_cmp_lt_i32_e64 s[48:49], v32, v125
	s_nop 1
	v_cndmask_b32_e64 v32, 1.0, v70, s[48:49]
	v_mul_f32_e32 v35, v35, v32
	v_mul_f32_e32 v61, v65, v35
	v_mul_f32_e32 v65, v33, v61
	v_mul_f32_e32 v66, v66, v65
	v_mul_f32_e32 v67, v67, v66
	v_mul_f32_e32 v68, v68, v67
	v_mul_f32_e32 v69, v69, v68
	v_mov_b32_e32 v87, v69
	v_mov_b32_e32 v70, v69
	s_nop 1
	v_permlane32_swap_b32 v87, v70
	v_mov_b32_e32 v86, v87
	v_mov_b32_e32 v33, v70
	s_nop 1
	v_permlane16_swap_b32 v86, v87
	v_permlane16_swap_b32 v33, v70
	s_nop 1
	s_and_saveexec_b64 s[88:89], vcc
	s_xor_b64 s[88:89], exec, s[88:89]
	s_and_b64 s[86:87], s[12:13], exec
	s_andn2_saveexec_b64 s[88:89], s[88:89]
	s_andn2_b64 s[68:69], s[86:87], exec
	s_and_b64 s[86:87], s[14:15], exec
	s_or_b64 s[86:87], s[68:69], s[86:87]
	s_mov_b64 s[68:69], exec
	s_or_b64 exec, exec, s[88:89]
	s_waitcnt lgkmcnt(0)
	v_mul_f32_e32 v88, v33, v70
	v_mov_b32_e32 v33, v88
	s_and_saveexec_b64 s[88:89], s[86:87]
	s_xor_b64 s[86:87], exec, s[88:89]
	v_cndmask_b32_e64 v33, 1.0, v70, s[10:11]
	s_andn2_b64 s[68:69], s[68:69], exec
	s_or_b64 exec, exec, s[86:87]
	s_and_saveexec_b64 s[86:87], s[68:69]
	v_mul_f32_e32 v33, v88, v87
	s_or_b64 exec, exec, s[86:87]
	s_and_b64 vcc, exec, s[8:9]
	s_cbranch_vccnz .LBB0_2004
	s_waitcnt vmcnt(3)
	ds_write_b128 v98, v[16:19] offset:16384
	s_waitcnt vmcnt(2)
	ds_write_b128 v99, v[20:23] offset:16384
	s_waitcnt vmcnt(1)
	ds_write_b128 v100, v[24:27] offset:32768
	s_waitcnt vmcnt(0)
	ds_write_b128 v124, v[28:31] offset:32768

.LBB0_2010:
	v_med3_f32 v64, v80, s55, v123
	v_exp_f32_e32 v66, v64
	v_med3_f32 v64, v81, s55, v123
	v_exp_f32_e32 v67, v64
	v_add_u32_e32 v80, s62, v126
	v_add_f32_e32 v64, 1.0, v66
	v_rcp_f32_e32 v64, v64
	v_add_u32_e32 v65, 32, v80
	v_add_f32_e32 v81, 1.0, v67
	v_cmp_lt_i32_e32 vcc, v65, v125
	v_med3_f32 v83, v83, s55, v123
	v_exp_f32_e32 v83, v83
	v_cndmask_b32_e32 v65, 1.0, v64, vcc
	v_rcp_f32_e32 v64, v81
	v_med3_f32 v81, v82, s55, v123
	v_exp_f32_e32 v82, v81
	v_add_u32_e32 v81, 33, v80
	v_cmp_lt_i32_e64 s[16:17], v81, v125
	v_add_u32_e32 v84, 34, v80
	v_cmp_lt_i32_e64 s[18:19], v84, v125
	v_cndmask_b32_e64 v81, 1.0, v64, s[16:17]
	v_add_f32_e32 v64, 1.0, v82
	v_rcp_f32_e32 v64, v64
	v_med3_f32 v76, v76, s55, v123
	v_exp_f32_e32 v76, v76
	v_add_u32_e32 v84, 35, v80
	v_cndmask_b32_e64 v94, 1.0, v64, s[18:19]
	v_add_f32_e32 v64, 1.0, v83
	v_rcp_f32_e32 v64, v64
	v_cmp_lt_i32_e64 s[20:21], v84, v125
	v_med3_f32 v77, v77, s55, v123
	v_exp_f32_e32 v77, v77
	v_cndmask_b32_e64 v92, 1.0, v64, s[20:21]
	v_add_f32_e32 v64, 1.0, v76
	v_rcp_f32_e32 v64, v64
	v_add_u32_e32 v84, 36, v80
	v_cmp_lt_i32_e64 s[22:23], v84, v125
	v_add_u32_e32 v84, 37, v80
	v_med3_f32 v78, v78, s55, v123
	v_cndmask_b32_e64 v91, 1.0, v64, s[22:23]
	v_add_f32_e32 v64, 1.0, v77
	v_rcp_f32_e32 v64, v64
	v_exp_f32_e32 v90, v78
	v_cmp_lt_i32_e64 s[24:25], v84, v125
	v_cmp_lt_i32_e64 s[30:31], 0, v127
	s_mov_b64 s[34:35], 0
	v_cndmask_b32_e64 v78, 1.0, v64, s[24:25]
	v_med3_f32 v64, v79, s55, v123
	v_exp_f32_e32 v93, v64
	v_add_f32_e32 v64, 1.0, v90
	v_rcp_f32_e32 v64, v64
	v_add_u32_e32 v79, 38, v80
	v_add_f32_e32 v84, 1.0, v93
	v_rcp_f32_e32 v84, v84
	v_cmp_lt_i32_e64 s[26:27], v79, v125
	s_mov_b64 s[36:37], 0
	s_nop 0
	v_cndmask_b32_e64 v79, 1.0, v64, s[26:27]
	v_add_u32_e32 v64, 39, v80
	v_cmp_lt_i32_e64 s[28:29], v64, v125
	s_nop 1
	v_cndmask_b32_e64 v64, 1.0, v84, s[28:29]
	v_mul_f32_e32 v84, v79, v64
	v_mul_f32_e32 v89, v78, v84
	v_mul_f32_e32 v91, v91, v89
	v_mul_f32_e32 v92, v92, v91
	v_mul_f32_e32 v94, v94, v92
	v_mul_f32_e32 v95, v81, v94
	v_mul_f32_e32 v96, v65, v95
	v_mov_b32_e32 v79, v96
	v_mov_b32_e32 v97, v96
	s_nop 1
	v_permlane32_swap_b32 v79, v97
	v_mov_b32_e32 v78, v79
	v_mov_b32_e32 v65, v97
	s_nop 1
	v_permlane16_swap_b32 v78, v79
	v_permlane16_swap_b32 v65, v97
	s_nop 1
	s_and_saveexec_b64 s[38:39], s[30:31]
	s_xor_b64 s[30:31], exec, s[38:39]
	s_and_b64 s[36:37], s[12:13], exec
	s_andn2_saveexec_b64 s[30:31], s[30:31]
	s_andn2_b64 s[34:35], s[36:37], exec
	s_and_b64 s[36:37], s[14:15], exec
	s_or_b64 s[36:37], s[34:35], s[36:37]
	s_mov_b64 s[34:35], exec
	s_or_b64 exec, exec, s[30:31]
	s_waitcnt lgkmcnt(0)
	v_mul_f32_e32 v81, v65, v97
	v_mov_b32_e32 v65, v81
	s_and_saveexec_b64 s[30:31], s[36:37]
	s_xor_b64 s[30:31], exec, s[30:31]
	v_cndmask_b32_e64 v65, 1.0, v97, s[10:11]
	s_andn2_b64 s[34:35], s[34:35], exec
	s_or_b64 exec, exec, s[30:31]
	s_and_saveexec_b64 s[30:31], s[34:35]
	v_mul_f32_e32 v65, v81, v79
	s_or_b64 exec, exec, s[30:31]
	v_cndmask_b32_e64 v155, 0, v77, s[24:25]
	v_mul_f32_e32 v77, v86, v87
	v_mul_f32_e32 v77, v77, v88
	v_cndmask_b32_e32 v66, 0, v66, vcc
	v_cndmask_b32_e64 v67, 0, v67, s[16:17]
	v_cndmask_b32_e64 v154, 0, v76, s[22:23]
	v_cndmask_b32_e64 v76, 0, v93, s[28:29]
	v_mul_f32_e32 v77, v85, v77
	v_cndmask_b32_e64 v97, 0, v82, s[18:19]
	v_cndmask_b32_e64 v153, 0, v83, s[20:21]
	v_pk_mul_f32 v[82:83], v[76:77], v[64:65]
	v_mul_f32_e32 v64, v66, v96
	v_mul_f32_e32 v65, v67, v95
	v_mul_f32_e32 v64, v64, v83
	v_mul_f32_e32 v65, v65, v83
	v_cvt_pk_bf16_f32 v64, v64, v65
	v_mul_f32_e32 v65, v97, v94
	v_mul_f32_e32 v66, v153, v92
	v_mul_f32_e32 v65, v65, v83
	v_mul_f32_e32 v66, v66, v83
	v_cvt_pk_bf16_f32 v65, v65, v66
	v_mul_f32_e32 v66, v154, v91
	v_mul_f32_e32 v67, v155, v89
	v_cndmask_b32_e64 v90, 0, v90, s[26:27]
	v_mul_f32_e32 v66, v66, v83
	v_mul_f32_e32 v67, v67, v83
	v_cvt_pk_bf16_f32 v66, v66, v67
	v_mul_f32_e32 v67, v90, v84
	v_mul_f32_e32 v67, v67, v83
	v_pk_mul_f32 v[82:83], v[82:83], v[82:83] op_sel_hi:[0,1]
	v_cvt_pk_bf16_f32 v67, v67, v83
	v_med3_f32 v72, v72, s55, v123
	v_exp_f32_e32 v72, v72
	v_med3_f32 v73, v73, s55, v123
	v_exp_f32_e32 v73, v73
	v_cmp_lt_i32_e64 s[16:17], v80, v125
	v_add_f32_e32 v76, 1.0, v72
	v_rcp_f32_e32 v76, v76
	v_add_f32_e32 v82, 1.0, v73
	v_rcp_f32_e32 v82, v82
	v_med3_f32 v74, v74, s55, v123
	v_cndmask_b32_e64 v84, 1.0, v76, s[16:17]
	v_or_b32_e32 v76, 1, v80
	v_exp_f32_e32 v74, v74
	v_cmp_lt_i32_e64 s[18:19], v76, v125
	v_med3_f32 v68, v68, s55, v123
	v_med3_f32 v75, v75, s55, v123
	v_cndmask_b32_e64 v89, 1.0, v82, s[18:19]
	v_or_b32_e32 v82, 2, v80
	v_cmp_lt_i32_e64 s[20:21], v82, v125
	v_exp_f32_e32 v82, v68
	v_add_f32_e32 v76, 1.0, v74
	v_rcp_f32_e32 v76, v76
	v_exp_f32_e32 v75, v75
	v_or_b32_e32 v68, 3, v80
	v_cmp_lt_i32_e64 s[22:23], v68, v125
	v_add_f32_e32 v68, 1.0, v82
	v_med3_f32 v69, v69, s55, v123
	v_rcp_f32_e32 v68, v68
	v_exp_f32_e32 v83, v69
	v_cndmask_b32_e64 v88, 1.0, v76, s[20:21]
	v_add_f32_e32 v76, 1.0, v75
	v_or_b32_e32 v69, 4, v80
	v_rcp_f32_e32 v76, v76
	v_cmp_lt_i32_e64 s[24:25], v69, v125
	v_med3_f32 v70, v70, s55, v123
	v_exp_f32_e32 v70, v70
	v_cndmask_b32_e64 v69, 1.0, v68, s[24:25]
	v_add_f32_e32 v68, 1.0, v83
	v_rcp_f32_e32 v68, v68
	v_cndmask_b32_e64 v87, 1.0, v76, s[22:23]
	v_or_b32_e32 v76, 5, v80
	v_cmp_lt_i32_e64 s[26:27], v76, v125
	v_cmp_lt_i32_e32 vcc, 0, v127
	s_mov_b64 s[34:35], 0
	v_cndmask_b32_e64 v85, 1.0, v68, s[26:27]
	v_med3_f32 v68, v71, s55, v123
	v_exp_f32_e32 v76, v68
	v_add_f32_e32 v68, 1.0, v70
	v_rcp_f32_e32 v68, v68
	v_or_b32_e32 v71, 6, v80
	v_add_f32_e32 v86, 1.0, v76
	v_rcp_f32_e32 v86, v86
	v_cmp_lt_i32_e64 s[28:29], v71, v125
	s_mov_b64 s[36:37], 0
	s_nop 0
	v_cndmask_b32_e64 v71, 1.0, v68, s[28:29]
	v_or_b32_e32 v68, 7, v80
	v_cmp_lt_i32_e64 s[30:31], v68, v125
	s_nop 1
	v_cndmask_b32_e64 v68, 1.0, v86, s[30:31]
	v_mul_f32_e32 v71, v71, v68
	v_mul_f32_e32 v85, v85, v71
	v_mul_f32_e32 v86, v69, v85
	v_mul_f32_e32 v87, v87, v86
	v_mul_f32_e32 v88, v88, v87
	v_mul_f32_e32 v89, v89, v88
	v_mul_f32_e32 v90, v84, v89
	v_mov_b32_e32 v84, v90
	v_mov_b32_e32 v69, v90
	s_nop 1
	v_permlane32_swap_b32 v84, v69
	v_mov_b32_e32 v80, v84
	v_mov_b32_e32 v91, v69
	s_nop 1
	v_permlane16_swap_b32 v80, v84
	v_permlane16_swap_b32 v91, v69
	s_nop 1
	s_and_saveexec_b64 s[38:39], vcc
	s_xor_b64 s[38:39], exec, s[38:39]
	s_and_b64 s[36:37], s[12:13], exec
	s_andn2_saveexec_b64 s[38:39], s[38:39]
	s_andn2_b64 s[34:35], s[36:37], exec
	s_and_b64 s[36:37], s[14:15], exec
	s_or_b64 s[36:37], s[34:35], s[36:37]
	s_mov_b64 s[34:35], exec
	s_or_b64 exec, exec, s[38:39]
	s_waitcnt lgkmcnt(0)
	v_mul_f32_e32 v91, v91, v69
	v_mov_b32_e32 v92, v91
	s_and_saveexec_b64 s[38:39], s[36:37]
	s_xor_b64 s[36:37], exec, s[38:39]
	v_cndmask_b32_e64 v92, 1.0, v69, s[10:11]
	s_andn2_b64 s[34:35], s[34:35], exec
	s_or_b64 exec, exec, s[36:37]
	s_and_saveexec_b64 s[36:37], s[34:35]
	v_mul_f32_e32 v92, v91, v84
	s_or_b64 exec, exec, s[36:37]
	s_and_b64 vcc, exec, s[8:9]
	s_cbranch_vccnz .LBB0_2028
	s_waitcnt vmcnt(3)
	ds_write_b128 v98, v[16:19]
	s_waitcnt vmcnt(2)
	ds_write_b128 v99, v[20:23]
	s_waitcnt vmcnt(1)
	ds_write_b128 v100, v[24:27] offset:49152
	s_waitcnt vmcnt(0)
	ds_write_b128 v124, v[28:31] offset:49152

.LBB0_2034:
	v_med3_f32 v66, v86, s55, v123
	v_med3_f32 v69, v81, s55, v123
	v_exp_f32_e32 v86, v66
	v_med3_f32 v66, v87, s55, v123
	v_exp_f32_e32 v89, v69
	v_med3_f32 v69, v82, s55, v123
	v_exp_f32_e32 v87, v66
	v_med3_f32 v66, v80, s55, v123
	v_exp_f32_e32 v80, v69
	v_med3_f32 v69, v83, s55, v123
	v_exp_f32_e32 v81, v69
	v_exp_f32_e32 v88, v66
	v_med3_f32 v64, v84, s55, v123
	v_exp_f32_e32 v84, v64
	v_med3_f32 v64, v85, s55, v123
	v_add_f32_e32 v70, 1.0, v80
	v_add_f32_e32 v71, 1.0, v81
	v_exp_f32_e32 v85, v64
	v_add_f32_e32 v69, 1.0, v89
	v_rcp_f32_e32 v70, v70
	v_rcp_f32_e32 v83, v71
	v_add_f32_e32 v68, 1.0, v88
	v_rcp_f32_e32 v69, v69
	v_add_f32_e32 v67, 1.0, v87
	v_rcp_f32_e32 v68, v68
	v_add_f32_e32 v66, 1.0, v86
	v_rcp_f32_e32 v67, v67
	v_add_f32_e32 v65, 1.0, v85
	v_rcp_f32_e32 v66, v66
	v_mul_f32_e32 v82, v70, v83
	v_add_f32_e32 v64, 1.0, v84
	v_rcp_f32_e32 v65, v65
	v_mul_f32_e32 v91, v69, v82
	v_rcp_f32_e32 v64, v64
	v_mul_f32_e32 v90, v68, v91
	v_mul_f32_e32 v93, v67, v90
	v_mul_f32_e32 v92, v66, v93
	v_mul_f32_e32 v95, v65, v92
	v_mul_f32_e32 v94, v64, v95
	v_mov_b32_e32 v71, v94
	v_mov_b32_e32 v64, v94
	s_nop 1
	v_permlane32_swap_b32 v71, v64
	v_mov_b32_e32 v70, v71
	v_mov_b32_e32 v65, v64
	s_nop 1
	v_permlane16_swap_b32 v70, v71
	v_permlane16_swap_b32 v65, v64
	s_nop 1
	s_waitcnt lgkmcnt(0)
	v_mul_f32_e32 v157, v65, v64
	v_mul_f32_e32 v246, v157, v71
	v_cndmask_b32_e64 v158, 1.0, v64, s[10:11]
	v_cndmask_b32_e64 v158, v246, v158, s[14:15]
	v_cndmask_b32_e64 v158, v157, v158, s[12:13]
	v_med3_f32 v64, v76, s55, v123
	v_exp_f32_e32 v66, v64
	v_med3_f32 v64, v77, s55, v123
	v_exp_f32_e32 v67, v64
	v_med3_f32 v72, v72, s55, v123
	v_add_f32_e32 v64, 1.0, v66
	v_rcp_f32_e32 v68, v64
	v_med3_f32 v64, v78, s55, v123
	v_exp_f32_e32 v64, v64
	v_exp_f32_e32 v76, v72
	v_add_f32_e32 v65, 1.0, v67
	v_rcp_f32_e32 v69, v65
	v_add_f32_e32 v72, 1.0, v64
	v_rcp_f32_e32 v96, v72
	v_med3_f32 v72, v73, s55, v123
	v_exp_f32_e32 v77, v72
	v_med3_f32 v72, v74, s55, v123
	v_exp_f32_e32 v72, v72
	v_med3_f32 v73, v75, s55, v123
	v_exp_f32_e32 v73, v73
	v_med3_f32 v65, v79, s55, v123
	v_exp_f32_e32 v65, v65
	v_add_f32_e32 v75, 1.0, v72
	v_rcp_f32_e32 v97, v75
	v_add_f32_e32 v75, 1.0, v73
	v_add_f32_e32 v74, 1.0, v77
	v_rcp_f32_e32 v75, v75
	v_add_f32_e32 v79, 1.0, v76
	v_rcp_f32_e32 v154, v74
	v_add_f32_e32 v78, 1.0, v65
	v_rcp_f32_e32 v155, v79
	v_rcp_f32_e32 v156, v78
	v_mul_f32_e32 v74, v97, v75
	v_mul_f32_e32 v79, v154, v74
	v_mul_f32_e32 v78, v155, v79
	v_mul_f32_e32 v97, v156, v78
	v_mul_f32_e32 v96, v96, v97
	v_mul_f32_e32 v69, v69, v96
	v_mul_f32_e32 v68, v68, v69
	v_mov_b32_e32 v155, v68
	v_mov_b32_e32 v160, v68
	s_nop 1
	v_permlane32_swap_b32 v155, v160
	v_mov_b32_e32 v154, v155
	v_mov_b32_e32 v156, v160
	s_nop 1
	v_permlane16_swap_b32 v154, v155
	v_permlane16_swap_b32 v156, v160
	s_nop 1
	s_waitcnt lgkmcnt(0)
	v_mul_f32_e32 v156, v156, v160
	v_mul_f32_e32 v246, v156, v155
	v_cndmask_b32_e64 v159, 1.0, v160, s[10:11]
	v_cndmask_b32_e64 v159, v246, v159, s[14:15]
	v_cndmask_b32_e64 v159, v156, v159, s[12:13]
	s_and_b64 vcc, exec, s[8:9]
	s_cbranch_vccnz .LBB0_2052
	s_waitcnt vmcnt(3)
	ds_write_b128 v98, v[16:19] offset:16384
	s_waitcnt vmcnt(2)
	ds_write_b128 v99, v[20:23] offset:16384
	s_waitcnt vmcnt(1)
	ds_write_b128 v100, v[24:27] offset:32768
	s_waitcnt vmcnt(0)
	ds_write_b128 v124, v[28:31] offset:32768

.LBB0_2058:
	v_med3_f32 v73, v73, s55, v123
	v_exp_f32_e32 v73, v73
	v_med3_f32 v78, v78, s55, v123
	v_exp_f32_e32 v78, v78
	v_med3_f32 v79, v79, s55, v123
	v_med3_f32 v72, v72, s55, v123
	v_med3_f32 v77, v77, s55, v123
	v_exp_f32_e32 v79, v79
	v_exp_f32_e32 v72, v72
	v_med3_f32 v74, v74, s55, v123
	v_med3_f32 v76, v76, s55, v123
	v_exp_f32_e32 v77, v77
	v_add_f32_e32 v81, 1.0, v73
	v_exp_f32_e32 v74, v74
	v_med3_f32 v75, v75, s55, v123
	v_exp_f32_e32 v76, v76
	v_rcp_f32_e32 v87, v81
	v_exp_f32_e32 v75, v75
	v_add_f32_e32 v81, 1.0, v78
	v_rcp_f32_e32 v85, v81
	v_add_f32_e32 v81, 1.0, v79
	v_add_f32_e32 v80, 1.0, v72
	v_add_f32_e32 v83, 1.0, v77
	v_rcp_f32_e32 v81, v81
	v_rcp_f32_e32 v86, v80
	v_add_f32_e32 v80, 1.0, v74
	v_add_f32_e32 v82, 1.0, v76
	v_rcp_f32_e32 v83, v83
	v_rcp_f32_e32 v84, v80
	v_add_f32_e32 v80, 1.0, v75
	v_rcp_f32_e32 v82, v82
	v_rcp_f32_e32 v88, v80
	v_mul_f32_e32 v80, v85, v81
	v_mul_f32_e32 v83, v83, v80
	v_mul_f32_e32 v82, v82, v83
	v_mul_f32_e32 v85, v88, v82
	v_mul_f32_e32 v84, v84, v85
	v_mul_f32_e32 v87, v87, v84
	v_mul_f32_e32 v86, v86, v87
	v_mov_b32_e32 v97, v86
	v_mov_b32_e32 v88, v86
	s_nop 1
	v_permlane32_swap_b32 v97, v88
	v_mov_b32_e32 v96, v97
	v_mov_b32_e32 v89, v88
	s_nop 1
	v_permlane16_swap_b32 v96, v97
	v_permlane16_swap_b32 v89, v88
	s_nop 1
	s_waitcnt lgkmcnt(0)
	v_mul_f32_e32 v159, v89, v88
	v_mul_f32_e32 v246, v159, v97
	v_cndmask_b32_e64 v158, 1.0, v88, s[10:11]
	v_cndmask_b32_e64 v158, v246, v158, s[14:15]
	v_cndmask_b32_e64 v158, v159, v158, s[12:13]
	v_med3_f32 v69, v69, s55, v123
	v_exp_f32_e32 v69, v69
	v_med3_f32 v66, v66, s55, v123
	v_exp_f32_e32 v66, v66
	v_med3_f32 v67, v67, s55, v123
	v_med3_f32 v68, v68, s55, v123
	v_med3_f32 v65, v65, s55, v123
	v_exp_f32_e32 v67, v67
	v_exp_f32_e32 v68, v68
	v_med3_f32 v70, v70, s55, v123
	v_med3_f32 v64, v64, s55, v123
	v_exp_f32_e32 v65, v65
	v_add_f32_e32 v89, 1.0, v69
	v_exp_f32_e32 v70, v70
	v_med3_f32 v71, v71, s55, v123
	v_exp_f32_e32 v64, v64
	v_rcp_f32_e32 v95, v89
	v_exp_f32_e32 v71, v71
	v_add_f32_e32 v89, 1.0, v66
	v_rcp_f32_e32 v93, v89
	v_add_f32_e32 v89, 1.0, v67
	v_add_f32_e32 v88, 1.0, v68
	v_add_f32_e32 v91, 1.0, v65
	v_rcp_f32_e32 v89, v89
	v_rcp_f32_e32 v94, v88
	v_add_f32_e32 v88, 1.0, v70
	v_add_f32_e32 v90, 1.0, v64
	v_rcp_f32_e32 v91, v91
	v_rcp_f32_e32 v92, v88
	v_add_f32_e32 v88, 1.0, v71
	v_rcp_f32_e32 v90, v90
	v_rcp_f32_e32 v160, v88
	v_mul_f32_e32 v88, v93, v89
	v_mul_f32_e32 v91, v91, v88
	v_mul_f32_e32 v90, v90, v91
	v_mul_f32_e32 v93, v160, v90
	v_mul_f32_e32 v92, v92, v93
	v_mul_f32_e32 v95, v95, v92
	v_mul_f32_e32 v94, v94, v95
	v_mov_b32_e32 v161, v94
	v_mov_b32_e32 v164, v94
	s_nop 1
	v_permlane32_swap_b32 v161, v164
	v_mov_b32_e32 v160, v161
	v_mov_b32_e32 v162, v164
	s_nop 1
	v_permlane16_swap_b32 v160, v161
	v_permlane16_swap_b32 v162, v164
	s_nop 1
	s_waitcnt lgkmcnt(0)
	v_mul_f32_e32 v162, v162, v164
	v_mul_f32_e32 v246, v162, v161
	v_cndmask_b32_e64 v163, 1.0, v164, s[10:11]
	v_cndmask_b32_e64 v163, v246, v163, s[14:15]
	v_cndmask_b32_e64 v163, v162, v163, s[12:13]
	s_and_b64 vcc, exec, s[8:9]
	s_cbranch_vccnz .LBB0_2076
	s_waitcnt vmcnt(3)
	ds_write_b128 v98, v[16:19]
	s_waitcnt vmcnt(2)
	ds_write_b128 v99, v[20:23]
	s_waitcnt vmcnt(1)
	ds_write_b128 v100, v[24:27] offset:49152
	s_waitcnt vmcnt(0)
	ds_write_b128 v124, v[28:31] offset:49152

.LBB0_2112:
	v_med3_f32 v72, v80, s55, v123
	v_exp_f32_e32 v80, v72
	v_med3_f32 v72, v81, s55, v123
	v_exp_f32_e32 v81, v72
	v_add_u32_e32 v75, s4, v126
	v_add_f32_e32 v72, 1.0, v80
	v_rcp_f32_e32 v72, v72
	v_add_u32_e32 v73, 32, v75
	v_add_f32_e32 v74, 1.0, v81
	v_cmp_lt_i32_e64 s[16:17], v73, v125
	v_med3_f32 v83, v83, s55, v123
	v_exp_f32_e32 v83, v83
	v_cndmask_b32_e64 v73, 1.0, v72, s[16:17]
	v_rcp_f32_e32 v72, v74
	v_med3_f32 v74, v82, s55, v123
	v_exp_f32_e32 v82, v74
	v_add_u32_e32 v74, 33, v75
	v_cmp_lt_i32_e64 s[18:19], v74, v125
	v_add_u32_e32 v84, 34, v75
	v_cmp_lt_i32_e64 s[20:21], v84, v125
	v_cndmask_b32_e64 v74, 1.0, v72, s[18:19]
	v_add_f32_e32 v72, 1.0, v82
	v_rcp_f32_e32 v72, v72
	v_med3_f32 v76, v76, s55, v123
	v_exp_f32_e32 v76, v76
	v_add_u32_e32 v84, 35, v75
	v_cndmask_b32_e64 v92, 1.0, v72, s[20:21]
	v_add_f32_e32 v72, 1.0, v83
	v_rcp_f32_e32 v72, v72
	v_cmp_lt_i32_e64 s[22:23], v84, v125
	v_med3_f32 v77, v77, s55, v123
	v_exp_f32_e32 v77, v77
	v_cndmask_b32_e64 v91, 1.0, v72, s[22:23]
	v_add_f32_e32 v72, 1.0, v76
	v_rcp_f32_e32 v72, v72
	v_add_u32_e32 v84, 36, v75
	v_cmp_lt_i32_e64 s[24:25], v84, v125
	v_add_u32_e32 v90, 37, v75
	v_med3_f32 v78, v78, s55, v123
	v_cndmask_b32_e64 v89, 1.0, v72, s[24:25]
	v_add_f32_e32 v72, 1.0, v77
	v_rcp_f32_e32 v72, v72
	v_exp_f32_e32 v84, v78
	v_cmp_lt_i32_e64 s[26:27], v90, v125
	v_add_u32_e32 v78, 38, v75
	v_cmp_lt_i32_e64 s[28:29], v78, v125
	v_cndmask_b32_e64 v93, 1.0, v72, s[26:27]
	v_med3_f32 v72, v79, s55, v123
	v_exp_f32_e32 v90, v72
	v_add_f32_e32 v72, 1.0, v84
	v_rcp_f32_e32 v72, v72
	v_cmp_lt_i32_e32 vcc, 0, v127
	v_add_f32_e32 v79, 1.0, v90
	v_rcp_f32_e32 v79, v79
	v_cndmask_b32_e64 v78, 1.0, v72, s[28:29]
	v_add_u32_e32 v72, 39, v75
	v_cmp_lt_i32_e64 s[30:31], v72, v125
	s_mov_b64 s[34:35], 0
	s_mov_b64 s[36:37], 0
	v_cndmask_b32_e64 v72, 1.0, v79, s[30:31]
	v_mul_f32_e32 v78, v78, v72
	v_mul_f32_e32 v79, v93, v78
	v_mul_f32_e32 v89, v89, v79
	v_mul_f32_e32 v91, v91, v89
	v_mul_f32_e32 v92, v92, v91
	v_mul_f32_e32 v93, v74, v92
	v_mul_f32_e32 v94, v73, v93
	v_mov_b32_e32 v95, v94
	v_mov_b32_e32 v97, v94
	s_nop 1
	v_permlane32_swap_b32 v95, v97
	v_mov_b32_e32 v74, v95
	v_mov_b32_e32 v73, v97
	s_nop 1
	v_permlane16_swap_b32 v74, v95
	v_permlane16_swap_b32 v73, v97
	s_nop 1
	s_and_saveexec_b64 s[4:5], vcc
	s_xor_b64 s[38:39], exec, s[4:5]
	s_and_b64 s[36:37], s[12:13], exec
	s_andn2_saveexec_b64 s[38:39], s[38:39]
	s_andn2_b64 s[4:5], s[36:37], exec
	s_and_b64 s[34:35], s[14:15], exec
	s_or_b64 s[36:37], s[4:5], s[34:35]
	s_mov_b64 s[34:35], exec
	s_or_b64 exec, exec, s[38:39]
	s_waitcnt lgkmcnt(0)
	v_mul_f32_e32 v96, v73, v97
	v_mov_b32_e32 v73, v96
	s_and_saveexec_b64 s[4:5], s[36:37]
	s_xor_b64 s[36:37], exec, s[4:5]
	v_cndmask_b32_e64 v73, 1.0, v97, s[10:11]
	s_andn2_b64 s[34:35], s[34:35], exec
	s_or_b64 exec, exec, s[36:37]
	s_and_saveexec_b64 s[36:37], s[34:35]
	v_mul_f32_e32 v73, v96, v95
	s_or_b64 exec, exec, s[36:37]
	v_med3_f32 v71, v71, s55, v123
	v_exp_f32_e32 v71, v71
	v_or_b32_e32 v155, 2, v75
	v_cmp_lt_i32_e64 s[38:39], v155, v125
	v_med3_f32 v64, v64, s55, v123
	v_add_f32_e32 v155, 1.0, v71
	v_rcp_f32_e32 v156, v155
	v_exp_f32_e32 v155, v64
	v_or_b32_e32 v64, 3, v75
	v_cmp_lt_i32_e64 s[40:41], v64, v125
	v_med3_f32 v65, v65, s55, v123
	v_add_f32_e32 v64, 1.0, v155
	v_cndmask_b32_e64 v160, 1.0, v156, s[40:41]
	v_rcp_f32_e32 v64, v64
	v_exp_f32_e32 v156, v65
	v_or_b32_e32 v65, 4, v75
	v_cmp_lt_i32_e64 s[42:43], v65, v125
	v_or_b32_e32 v157, 5, v75
	v_med3_f32 v66, v66, s55, v123
	v_cndmask_b32_e64 v65, 1.0, v64, s[42:43]
	v_add_f32_e32 v64, 1.0, v156
	v_rcp_f32_e32 v64, v64
	v_exp_f32_e32 v66, v66
	v_cmp_lt_i32_e64 s[44:45], v157, v125
	v_med3_f32 v70, v70, s55, v123
	v_med3_f32 v69, v69, s55, v123
	v_cndmask_b32_e64 v157, 1.0, v64, s[44:45]
	v_med3_f32 v64, v67, s55, v123
	v_exp_f32_e32 v158, v64
	v_add_f32_e32 v64, 1.0, v66
	v_rcp_f32_e32 v64, v64
	v_exp_f32_e32 v70, v70
	v_add_f32_e32 v159, 1.0, v158
	v_med3_f32 v68, v68, s55, v123
	v_exp_f32_e32 v69, v69
	v_or_b32_e32 v67, 6, v75
	v_rcp_f32_e32 v159, v159
	v_exp_f32_e32 v68, v68
	v_cmp_lt_i32_e64 s[46:47], v67, v125
	v_or_b32_e32 v154, 1, v75
	v_cmp_lt_i32_e64 s[36:37], v154, v125
	v_cndmask_b32_e64 v67, 1.0, v64, s[46:47]
	v_or_b32_e32 v64, 7, v75
	v_add_f32_e32 v154, 1.0, v70
	v_cmp_lt_i32_e64 s[48:49], v64, v125
	v_add_f32_e32 v153, 1.0, v69
	v_rcp_f32_e32 v154, v154
	v_cndmask_b32_e64 v64, 1.0, v159, s[48:49]
	v_add_f32_e32 v97, 1.0, v68
	v_rcp_f32_e32 v153, v153
	v_mul_f32_e32 v67, v67, v64
	v_rcp_f32_e32 v97, v97
	v_mul_f32_e32 v157, v157, v67
	v_mul_f32_e32 v159, v65, v157
	v_cndmask_b32_e64 v154, 1.0, v154, s[38:39]
	v_mul_f32_e32 v160, v160, v159
	v_cmp_lt_i32_e64 s[34:35], v75, v125
	v_cndmask_b32_e64 v153, 1.0, v153, s[36:37]
	v_mul_f32_e32 v161, v154, v160
	v_cndmask_b32_e64 v97, 1.0, v97, s[34:35]
	v_mul_f32_e32 v162, v153, v161
	v_mul_f32_e32 v163, v97, v162
	v_mov_b32_e32 v153, v163
	v_mov_b32_e32 v65, v163
	s_nop 1
	v_permlane32_swap_b32 v153, v65
	v_mov_b32_e32 v97, v153
	v_mov_b32_e32 v75, v65
	s_nop 1
	v_permlane16_swap_b32 v97, v153
	v_permlane16_swap_b32 v75, v65
	s_nop 1
	v_cmp_lt_i32_e32 vcc, 0, v127
	s_mov_b64 s[68:69], 0
	s_mov_b64 s[86:87], 0
	s_and_saveexec_b64 s[4:5], vcc
	s_xor_b64 s[88:89], exec, s[4:5]
	s_and_b64 s[86:87], s[12:13], exec
	s_andn2_saveexec_b64 s[88:89], s[88:89]
	s_andn2_b64 s[4:5], s[86:87], exec
	s_and_b64 s[68:69], s[14:15], exec
	s_or_b64 s[86:87], s[4:5], s[68:69]
	s_mov_b64 s[68:69], exec
	s_or_b64 exec, exec, s[88:89]
	s_waitcnt lgkmcnt(0)
	v_mul_f32_e32 v154, v75, v65
	v_mov_b32_e32 v164, v154
	s_and_saveexec_b64 s[4:5], s[86:87]
	s_xor_b64 s[86:87], exec, s[4:5]
	v_cndmask_b32_e64 v164, 1.0, v65, s[10:11]
	s_andn2_b64 s[68:69], s[68:69], exec
	s_or_b64 exec, exec, s[86:87]
	s_and_saveexec_b64 s[86:87], s[68:69]
	v_mul_f32_e32 v164, v154, v153
	s_or_b64 exec, exec, s[86:87]
	s_and_b64 vcc, exec, s[8:9]
	s_cbranch_vccnz .LBB0_2130
	s_waitcnt vmcnt(3)
	ds_write_b128 v98, v[16:19]
	s_waitcnt vmcnt(2)
	ds_write_b128 v99, v[20:23]
	s_waitcnt vmcnt(1)
	ds_write_b128 v100, v[24:27] offset:49152
	s_waitcnt vmcnt(0)
	ds_write_b128 v124, v[28:31] offset:49152

.LBB0_2161:
	v_med3_f32 v73, v73, s55, v123
	v_exp_f32_e32 v73, v73
	v_med3_f32 v78, v78, s55, v123
	v_exp_f32_e32 v78, v78
	v_med3_f32 v79, v79, s55, v123
	v_med3_f32 v72, v72, s55, v123
	v_med3_f32 v77, v77, s55, v123
	v_exp_f32_e32 v79, v79
	v_exp_f32_e32 v72, v72
	v_med3_f32 v74, v74, s55, v123
	v_med3_f32 v76, v76, s55, v123
	v_exp_f32_e32 v77, v77
	v_add_f32_e32 v81, 1.0, v73
	v_exp_f32_e32 v74, v74
	v_med3_f32 v75, v75, s55, v123
	v_exp_f32_e32 v76, v76
	v_rcp_f32_e32 v87, v81
	v_exp_f32_e32 v75, v75
	v_add_f32_e32 v81, 1.0, v78
	v_rcp_f32_e32 v85, v81
	v_add_f32_e32 v81, 1.0, v79
	v_add_f32_e32 v80, 1.0, v72
	v_add_f32_e32 v83, 1.0, v77
	v_rcp_f32_e32 v81, v81
	v_rcp_f32_e32 v86, v80
	v_add_f32_e32 v80, 1.0, v74
	v_add_f32_e32 v82, 1.0, v76
	v_rcp_f32_e32 v83, v83
	v_rcp_f32_e32 v84, v80
	v_add_f32_e32 v80, 1.0, v75
	v_rcp_f32_e32 v82, v82
	v_rcp_f32_e32 v88, v80
	v_mul_f32_e32 v80, v85, v81
	v_mul_f32_e32 v83, v83, v80
	v_mul_f32_e32 v82, v82, v83
	v_mul_f32_e32 v85, v88, v82
	v_mul_f32_e32 v84, v84, v85
	v_mul_f32_e32 v87, v87, v84
	v_mul_f32_e32 v86, v86, v87
	v_mov_b32_e32 v97, v86
	v_mov_b32_e32 v88, v86
	s_nop 1
	v_permlane32_swap_b32 v97, v88
	v_mov_b32_e32 v96, v97
	v_mov_b32_e32 v89, v88
	s_nop 1
	v_permlane16_swap_b32 v96, v97
	v_permlane16_swap_b32 v89, v88
	s_nop 1
	s_waitcnt lgkmcnt(0)
	v_mul_f32_e32 v159, v89, v88
	v_mul_f32_e32 v246, v159, v97
	v_cndmask_b32_e64 v158, 1.0, v88, s[10:11]
	v_cndmask_b32_e64 v158, v246, v158, s[14:15]
	v_cndmask_b32_e64 v158, v159, v158, s[12:13]
	v_med3_f32 v69, v69, s55, v123
	v_exp_f32_e32 v69, v69
	v_med3_f32 v68, v68, s55, v123
	v_exp_f32_e32 v68, v68
	v_med3_f32 v65, v65, s55, v123
	v_add_f32_e32 v89, 1.0, v69
	v_rcp_f32_e32 v161, v89
	v_exp_f32_e32 v89, v65
	v_med3_f32 v65, v66, s55, v123
	v_exp_f32_e32 v90, v65
	v_med3_f32 v65, v67, s55, v123
	v_exp_f32_e32 v91, v65
	v_add_f32_e32 v88, 1.0, v68
	v_med3_f32 v64, v64, s55, v123
	v_rcp_f32_e32 v160, v88
	v_med3_f32 v71, v71, s55, v123
	v_exp_f32_e32 v88, v64
	v_med3_f32 v70, v70, s55, v123
	v_exp_f32_e32 v71, v71
	v_exp_f32_e32 v70, v70
	v_add_f32_e32 v66, 1.0, v90
	v_add_f32_e32 v67, 1.0, v91
	v_add_f32_e32 v65, 1.0, v89
	v_rcp_f32_e32 v66, v66
	v_rcp_f32_e32 v93, v67
	v_add_f32_e32 v94, 1.0, v88
	v_rcp_f32_e32 v65, v65
	v_add_f32_e32 v92, 1.0, v71
	v_rcp_f32_e32 v94, v94
	v_add_f32_e32 v64, 1.0, v70
	v_rcp_f32_e32 v95, v92
	v_rcp_f32_e32 v64, v64
	v_mul_f32_e32 v92, v66, v93
	v_mul_f32_e32 v67, v65, v92
	v_mul_f32_e32 v66, v94, v67
	v_mul_f32_e32 v95, v95, v66
	v_mul_f32_e32 v94, v64, v95
	v_mul_f32_e32 v65, v161, v94
	v_mul_f32_e32 v64, v160, v65
	v_mov_b32_e32 v161, v64
	v_mov_b32_e32 v164, v64
	s_nop 1
	v_permlane32_swap_b32 v161, v164
	v_mov_b32_e32 v160, v161
	v_mov_b32_e32 v162, v164
	s_nop 1
	v_permlane16_swap_b32 v160, v161
	v_permlane16_swap_b32 v162, v164
	s_nop 1
	s_waitcnt lgkmcnt(0)
	v_mul_f32_e32 v162, v162, v164
	v_mul_f32_e32 v246, v162, v161
	v_cndmask_b32_e64 v163, 1.0, v164, s[10:11]
	v_cndmask_b32_e64 v163, v246, v163, s[14:15]
	v_cndmask_b32_e64 v163, v162, v163, s[12:13]
	s_and_b64 vcc, exec, s[8:9]
	s_cbranch_vccnz .LBB0_2179
	s_waitcnt vmcnt(3)
	ds_write_b128 v98, v[16:19]
	s_waitcnt vmcnt(2)
	ds_write_b128 v99, v[20:23]
	s_waitcnt vmcnt(1)
	ds_write_b128 v100, v[24:27] offset:49152
	s_waitcnt vmcnt(0)
	ds_write_b128 v124, v[28:31] offset:49152
